# GEMM K-loops (6 of 7): counter/pointer/exit-test SALU moved in front of the iteration's last s_barrier (docs 7.11)
# speedup vs baseline: 1.0062x; 1.0062x over previous
; #define PG8_STAGE_A(bufoff, kt, h, usenext) do { if constexpr (Sched::GATHER) { unsigned vo_[2] = { (usenext) ? goffN[h][0] : goff[h][0], (usenext) ? goffN[h][1] : goff[h][1] }; PG8_STAGE(bufoff, kt, vo_); } \
;         else { PG8_STAGE(bufoff, (kt) + ((h) ? hstep : 0), voffA); } } while (0)
; #define PG8_STAGE(bufoff, gbase, voff) do { _Pragma("unroll") for (int _i = 0; _i < 2; ++_i) \
;         __builtin_amdgcn_global_load_lds((const unsigned*)((const char*)(gbase) + (voff)[_i]), (LAS unsigned*)(lds + (bufoff) + ldsw + _i * 8192), 16, 0, 0); } while (0)
; #define PG8_LDA(dst, b, h) do { _Pragma("unroll") for (int m = 0; m < 4; ++m) _Pragma("unroll") for (int k = 0; k < 2; ++k) dst[m][k] = *(const LAS bf16x8*)(lds + PG8_SA(b, h) + aoff + m * 2048 + k * 1024); } while (0)
; #define PG8_LDB(dst, b, h) do { _Pragma("unroll") for (int n = 0; n < 2; ++n) _Pragma("unroll") for (int k = 0; k < 2; ++k) dst[n][k] = *(const LAS bf16x8*)(lds + PG8_SB(b, h) + boff + n * 2048 + k * 1024); } while (0)
; #define PG8_MMA(ai, bj, At, Bt) do { __builtin_amdgcn_s_setprio(1); _Pragma("unroll") for (int m = 0; m < 4; ++m) _Pragma("unroll") for (int n = 0; n < 2; ++n) _Pragma("unroll") for (int k = 0; k < 2; ++k) \
;         acc[ai][bj][m][n] = __builtin_amdgcn_mfma_f32_16x16x32_bf16(Bt[n][k], At[m][k], acc[ai][bj][m][n], 0, 0, 0); __builtin_amdgcn_s_setprio(0); } while (0)
; #define PG8_WAIT_V(n) asm volatile("s_waitcnt vmcnt(" #n ")" ::: "memory")
; template <class Epi, class Sched, bool ALIGN_EPI = true, bool SP2 = true>
; __device__ __forceinline__ void gemm_phase(LAS unsigned char* lds, const Gemm g, const Sched& S, const Epi& E, int tid_in) {
;     ...
;             const char* a1 = cA + (size_t)(t + 1) * kstep;
;             const char* a2 = last ? nA : cA + (size_t)(t + 2) * kstep; const char* b2 = last ? nB : cB + (size_t)(t + 2) * kstep;
;             const char* a3 = a2 + kstep; const char* b3 = b2 + kstep;
;             if constexpr (SP2) {
;             PG8_LDB(B0, 0, 0); PG8_LDB(B1, 0, 1); PG8_SCHED; PG8_LDA(At, 0, 0); PG8_STAGE_A(PG8_SA(1, 1), a1, 1, false);
;             PG8_WAIT_V(8); PG8_WAIT_L(0); PG8_BAR; PG8_MMA(0, 0, At, B0); PG8_MMA(0, 1, At, B1); PG8_BAR; PG8_SCHED;
;             PG8_LDA(At, 0, 1); PG8_STAGE(PG8_SB(0, 0), b2, voffB); PG8_STAGE(PG8_SB(0, 1), b2 + hstepB, voffB); PG8_STAGE_A(PG8_SA(0, 0), a2, 0, last);
.LBB0_717:
	v_add_u32_e32 v156, s24, v141
	v_add_u32_e32 v172, s25, v141
	ds_read_b128 v[144:147], v156
	ds_read_b128 v[148:151], v156 offset:1024
	ds_read_b128 v[152:155], v156 offset:2048
	ds_read_b128 v[156:159], v156 offset:3072
	ds_read_b128 v[160:163], v172
	ds_read_b128 v[164:167], v172 offset:1024
	ds_read_b128 v[168:171], v172 offset:2048
	ds_read_b128 v[172:175], v172 offset:3072
	s_add_u32 s20, s18, 0xfffc0080
	s_addc_u32 s21, s19, -1
	s_cmp_eq_u32 s55, 12
	s_cselect_b32 s23, s13, s21
	s_cselect_b32 s22, s51, s20
	s_cselect_b32 s21, s11, s54
	s_cselect_b32 s20, s52, s53
	v_lshl_add_u64 v[208:209], s[18:19], 0, v[136:137]
	s_add_i32 m0, s34, 0xc000
	ds_read_b128 v[176:179], v143
	ds_read_b128 v[180:183], v143 offset:1024
	ds_read_b128 v[184:187], v143 offset:2048
	ds_read_b128 v[188:191], v143 offset:3072
	ds_read_b128 v[192:195], v143 offset:4096
	ds_read_b128 v[196:199], v143 offset:5120
	ds_read_b128 v[200:203], v143 offset:6144
	ds_read_b128 v[204:207], v143 offset:7168
	global_load_lds_dwordx4 v[208:209], off
	v_lshl_add_u64 v[208:209], s[18:19], 0, v[138:139]
	s_add_i32 m0, s34, 0xe000
	s_nop 0
	global_load_lds_dwordx4 v[208:209], off
	s_waitcnt vmcnt(8)
	s_waitcnt lgkmcnt(0)
	s_barrier
	s_setprio 1
	s_waitcnt lgkmcnt(0)
	v_mfma_f32_16x16x32_bf16 v[126:129], v[144:147], v[176:179], v[126:129]
	v_mfma_f32_16x16x32_bf16 v[122:125], v[152:155], v[176:179], v[122:125]
	v_mfma_f32_16x16x32_bf16 v[118:121], v[144:147], v[184:187], v[118:121]
	v_mfma_f32_16x16x32_bf16 v[114:117], v[152:155], v[184:187], v[114:117]
	v_mfma_f32_16x16x32_bf16 v[102:105], v[144:147], v[192:195], v[102:105]
	v_mfma_f32_16x16x32_bf16 v[98:101], v[152:155], v[192:195], v[98:101]
	v_mfma_f32_16x16x32_bf16 v[86:89], v[144:147], v[200:203], v[86:89]
	v_mfma_f32_16x16x32_bf16 v[82:85], v[152:155], v[200:203], v[82:85]
	v_mfma_f32_16x16x32_bf16 v[126:129], v[148:151], v[180:183], v[126:129]
	v_mfma_f32_16x16x32_bf16 v[122:125], v[156:159], v[180:183], v[122:125]
	v_mfma_f32_16x16x32_bf16 v[118:121], v[148:151], v[188:191], v[118:121]
	v_mfma_f32_16x16x32_bf16 v[114:117], v[156:159], v[188:191], v[114:117]
	v_mfma_f32_16x16x32_bf16 v[102:105], v[148:151], v[196:199], v[102:105]
	v_mfma_f32_16x16x32_bf16 v[98:101], v[156:159], v[196:199], v[98:101]
	v_mfma_f32_16x16x32_bf16 v[86:89], v[148:151], v[204:207], v[86:89]
	v_mfma_f32_16x16x32_bf16 v[82:85], v[156:159], v[204:207], v[82:85]
	s_setprio 0
	s_setprio 1
	v_mfma_f32_16x16x32_bf16 v[110:113], v[160:163], v[176:179], v[110:113]
	v_mfma_f32_16x16x32_bf16 v[106:109], v[168:171], v[176:179], v[106:109]
	v_mfma_f32_16x16x32_bf16 v[94:97], v[160:163], v[184:187], v[94:97]
	v_mfma_f32_16x16x32_bf16 v[90:93], v[168:171], v[184:187], v[90:93]
	v_mfma_f32_16x16x32_bf16 v[78:81], v[160:163], v[192:195], v[78:81]
	v_mfma_f32_16x16x32_bf16 v[74:77], v[168:171], v[192:195], v[74:77]
	v_mfma_f32_16x16x32_bf16 v[70:73], v[160:163], v[200:203], v[70:73]
	v_mfma_f32_16x16x32_bf16 v[66:69], v[168:171], v[200:203], v[66:69]
	v_mfma_f32_16x16x32_bf16 v[110:113], v[164:167], v[180:183], v[110:113]
	v_mfma_f32_16x16x32_bf16 v[106:109], v[172:175], v[180:183], v[106:109]
	v_mfma_f32_16x16x32_bf16 v[94:97], v[164:167], v[188:191], v[94:97]
	v_mfma_f32_16x16x32_bf16 v[90:93], v[172:175], v[188:191], v[90:93]
	v_mfma_f32_16x16x32_bf16 v[78:81], v[164:167], v[196:199], v[78:81]
	v_mfma_f32_16x16x32_bf16 v[74:77], v[172:175], v[196:199], v[74:77]
	v_mfma_f32_16x16x32_bf16 v[70:73], v[164:167], v[204:207], v[70:73]
	v_mfma_f32_16x16x32_bf16 v[66:69], v[172:175], v[204:207], v[66:69]
	s_setprio 0
	s_barrier
	s_mov_b32 m0, s9
	v_lshl_add_u64 v[208:209], s[20:21], 0, v[64:65]
	s_add_u32 s56, s20, 0x40000
	ds_read_b128 v[176:179], v143 offset:16384
	ds_read_b128 v[180:183], v143 offset:17408
	ds_read_b128 v[184:187], v143 offset:18432
	ds_read_b128 v[188:191], v143 offset:19456
	ds_read_b128 v[192:195], v143 offset:20480
	ds_read_b128 v[196:199], v143 offset:21504
	ds_read_b128 v[200:203], v143 offset:22528
	ds_read_b128 v[204:207], v143 offset:23552
	global_load_lds_dwordx4 v[208:209], off
	v_lshl_add_u64 v[210:211], s[20:21], 0, v[130:131]
	s_mov_b32 m0, s30
	s_addc_u32 s57, s21, 0
	global_load_lds_dwordx4 v[210:211], off
	v_lshl_add_u64 v[212:213], s[56:57], 0, v[64:65]
	s_mov_b32 m0, s31
	v_lshl_add_u64 v[214:215], s[22:23], 0, v[132:133]
	global_load_lds_dwordx4 v[212:213], off
	v_lshl_add_u64 v[212:213], s[56:57], 0, v[130:131]
	s_mov_b32 m0, s33
	s_nop 0
	global_load_lds_dwordx4 v[212:213], off
	v_lshl_add_u64 v[212:213], s[22:23], 0, v[134:135]
	s_mov_b32 m0, s34
	s_nop 0
	global_load_lds_dwordx4 v[212:213], off
	s_mov_b32 m0, s35
	s_nop 0
	global_load_lds_dwordx4 v[214:215], off
	s_waitcnt vmcnt(8)
	s_waitcnt lgkmcnt(0)
	s_barrier
; #define PG8_STAGE_A(bufoff, kt, h, usenext) do { if constexpr (Sched::GATHER) { unsigned vo_[2] = { (usenext) ? goffN[h][0] : goff[h][0], (usenext) ? goffN[h][1] : goff[h][1] }; PG8_STAGE(bufoff, kt, vo_); } \
;         else { PG8_STAGE(bufoff, (kt) + ((h) ? hstep : 0), voffA); } } while (0)
; #define PG8_LDA(dst, b, h) do { _Pragma("unroll") for (int m = 0; m < 4; ++m) _Pragma("unroll") for (int k = 0; k < 2; ++k) dst[m][k] = *(const LAS bf16x8*)(lds + PG8_SA(b, h) + aoff + m * 2048 + k * 1024); } while (0)
; #define PG8_LDB(dst, b, h) do { _Pragma("unroll") for (int n = 0; n < 2; ++n) _Pragma("unroll") for (int k = 0; k < 2; ++k) dst[n][k] = *(const LAS bf16x8*)(lds + PG8_SB(b, h) + boff + n * 2048 + k * 1024); } while (0)
; #define PG8_MMA(ai, bj, At, Bt) do { __builtin_amdgcn_s_setprio(1); _Pragma("unroll") for (int m = 0; m < 4; ++m) _Pragma("unroll") for (int n = 0; n < 2; ++n) _Pragma("unroll") for (int k = 0; k < 2; ++k) \
;         acc[ai][bj][m][n] = __builtin_amdgcn_mfma_f32_16x16x32_bf16(Bt[n][k], At[m][k], acc[ai][bj][m][n], 0, 0, 0); __builtin_amdgcn_s_setprio(0); } while (0)
; #define PG8_WAIT_V(n) asm volatile("s_waitcnt vmcnt(" #n ")" ::: "memory")
; #define PG8_WAIT_L(n) asm volatile("s_waitcnt lgkmcnt(" #n ")" ::: "memory")
; #define PG8_BAR __builtin_amdgcn_s_barrier()
; #define PG8_SCHED __builtin_amdgcn_sched_barrier(0)
; template <class Epi, class Sched, bool ALIGN_EPI = true, bool SP2 = true>
; __device__ __forceinline__ void gemm_phase(LAS unsigned char* lds, const Gemm g, const Sched& S, const Epi& E, int tid_in) {
;     ...
;             PG8_WAIT_V(8); PG8_WAIT_L(0); PG8_BAR; PG8_MMA(1, 0, At, B0); PG8_MMA(1, 1, At, B1); PG8_BAR; PG8_SCHED;
;             PG8_LDB(B0, 1, 0); PG8_LDB(B1, 1, 1); PG8_SCHED; PG8_LDA(At, 1, 0); PG8_STAGE_A(PG8_SA(0, 1), a2, 1, last);
;             PG8_WAIT_V(8); PG8_WAIT_L(0); PG8_BAR; PG8_MMA(0, 0, At, B0); PG8_MMA(0, 1, At, B1); PG8_BAR; PG8_SCHED;
	s_setprio 1
	s_waitcnt lgkmcnt(0)
	v_mfma_f32_16x16x32_bf16 v[60:63], v[144:147], v[176:179], v[60:63]
	v_mfma_f32_16x16x32_bf16 v[56:59], v[152:155], v[176:179], v[56:59]
	v_mfma_f32_16x16x32_bf16 v[52:55], v[144:147], v[184:187], v[52:55]
	v_mfma_f32_16x16x32_bf16 v[48:51], v[152:155], v[184:187], v[48:51]
	v_mfma_f32_16x16x32_bf16 v[36:39], v[144:147], v[192:195], v[36:39]
	v_mfma_f32_16x16x32_bf16 v[32:35], v[152:155], v[192:195], v[32:35]
	v_mfma_f32_16x16x32_bf16 v[20:23], v[144:147], v[200:203], v[20:23]
	v_mfma_f32_16x16x32_bf16 v[16:19], v[152:155], v[200:203], v[16:19]
	v_mfma_f32_16x16x32_bf16 v[60:63], v[148:151], v[180:183], v[60:63]
	v_mfma_f32_16x16x32_bf16 v[56:59], v[156:159], v[180:183], v[56:59]
	v_mfma_f32_16x16x32_bf16 v[52:55], v[148:151], v[188:191], v[52:55]
	v_mfma_f32_16x16x32_bf16 v[48:51], v[156:159], v[188:191], v[48:51]
	v_mfma_f32_16x16x32_bf16 v[36:39], v[148:151], v[196:199], v[36:39]
	v_mfma_f32_16x16x32_bf16 v[32:35], v[156:159], v[196:199], v[32:35]
	v_mfma_f32_16x16x32_bf16 v[20:23], v[148:151], v[204:207], v[20:23]
	v_mfma_f32_16x16x32_bf16 v[16:19], v[156:159], v[204:207], v[16:19]
	s_setprio 0
	s_setprio 1
	v_mfma_f32_16x16x32_bf16 v[44:47], v[160:163], v[176:179], v[44:47]
	v_mfma_f32_16x16x32_bf16 v[40:43], v[168:171], v[176:179], v[40:43]
	v_mfma_f32_16x16x32_bf16 v[28:31], v[160:163], v[184:187], v[28:31]
	v_mfma_f32_16x16x32_bf16 v[24:27], v[168:171], v[184:187], v[24:27]
	v_mfma_f32_16x16x32_bf16 v[12:15], v[160:163], v[192:195], v[12:15]
	v_mfma_f32_16x16x32_bf16 v[8:11], v[168:171], v[192:195], v[8:11]
	v_mfma_f32_16x16x32_bf16 v[4:7], v[160:163], v[200:203], v[4:7]
	v_mfma_f32_16x16x32_bf16 v[0:3], v[168:171], v[200:203], v[0:3]
	v_mfma_f32_16x16x32_bf16 v[44:47], v[164:167], v[180:183], v[44:47]
	v_mfma_f32_16x16x32_bf16 v[40:43], v[172:175], v[180:183], v[40:43]
	v_mfma_f32_16x16x32_bf16 v[28:31], v[164:167], v[188:191], v[28:31]
	v_mfma_f32_16x16x32_bf16 v[24:27], v[172:175], v[188:191], v[24:27]
	v_mfma_f32_16x16x32_bf16 v[12:15], v[164:167], v[196:199], v[12:15]
	v_mfma_f32_16x16x32_bf16 v[8:11], v[172:175], v[196:199], v[8:11]
	v_mfma_f32_16x16x32_bf16 v[4:7], v[164:167], v[204:207], v[4:7]
	v_mfma_f32_16x16x32_bf16 v[0:3], v[172:175], v[204:207], v[0:3]
	s_setprio 0
	s_barrier
	v_add_u32_e32 v156, s38, v141
	v_add_u32_e32 v172, s39, v141
	ds_read_b128 v[144:147], v156
	ds_read_b128 v[148:151], v156 offset:1024
	ds_read_b128 v[152:155], v156 offset:2048
	ds_read_b128 v[156:159], v156 offset:3072
	ds_read_b128 v[160:163], v172
	ds_read_b128 v[164:167], v172 offset:1024
	ds_read_b128 v[168:171], v172 offset:2048
	ds_read_b128 v[172:175], v172 offset:3072
	s_add_u32 s22, s22, 0x40000
	s_addc_u32 s23, s23, 0
	s_mov_b32 m0, s36
	v_lshl_add_u64 v[216:217], s[22:23], 0, v[134:135]
	ds_read_b128 v[176:179], v143 offset:32768
	ds_read_b128 v[180:183], v143 offset:33792
	ds_read_b128 v[184:187], v143 offset:34816
	ds_read_b128 v[188:191], v143 offset:35840
	ds_read_b128 v[192:195], v143 offset:36864
	ds_read_b128 v[196:199], v143 offset:37888
	ds_read_b128 v[200:203], v143 offset:38912
	ds_read_b128 v[204:207], v143 offset:39936
	global_load_lds_dwordx4 v[216:217], off
	v_lshl_add_u64 v[216:217], s[22:23], 0, v[132:133]
	s_mov_b32 m0, s37
	s_nop 0
	global_load_lds_dwordx4 v[216:217], off
	s_waitcnt vmcnt(8)
	s_waitcnt lgkmcnt(0)
	s_barrier
	s_setprio 1
	s_waitcnt lgkmcnt(0)
	v_mfma_f32_16x16x32_bf16 v[126:129], v[144:147], v[176:179], v[126:129]
	v_mfma_f32_16x16x32_bf16 v[122:125], v[152:155], v[176:179], v[122:125]
	v_mfma_f32_16x16x32_bf16 v[118:121], v[144:147], v[184:187], v[118:121]
	v_mfma_f32_16x16x32_bf16 v[114:117], v[152:155], v[184:187], v[114:117]
	v_mfma_f32_16x16x32_bf16 v[102:105], v[144:147], v[192:195], v[102:105]
	v_mfma_f32_16x16x32_bf16 v[98:101], v[152:155], v[192:195], v[98:101]
	v_mfma_f32_16x16x32_bf16 v[86:89], v[144:147], v[200:203], v[86:89]
	v_mfma_f32_16x16x32_bf16 v[82:85], v[152:155], v[200:203], v[82:85]
	v_mfma_f32_16x16x32_bf16 v[126:129], v[148:151], v[180:183], v[126:129]
	v_mfma_f32_16x16x32_bf16 v[122:125], v[156:159], v[180:183], v[122:125]
	v_mfma_f32_16x16x32_bf16 v[118:121], v[148:151], v[188:191], v[118:121]
	v_mfma_f32_16x16x32_bf16 v[114:117], v[156:159], v[188:191], v[114:117]
	v_mfma_f32_16x16x32_bf16 v[102:105], v[148:151], v[196:199], v[102:105]
	v_mfma_f32_16x16x32_bf16 v[98:101], v[156:159], v[196:199], v[98:101]
	v_mfma_f32_16x16x32_bf16 v[86:89], v[148:151], v[204:207], v[86:89]
	v_mfma_f32_16x16x32_bf16 v[82:85], v[156:159], v[204:207], v[82:85]
	s_setprio 0
	s_setprio 1
	v_mfma_f32_16x16x32_bf16 v[110:113], v[160:163], v[176:179], v[110:113]
	v_mfma_f32_16x16x32_bf16 v[106:109], v[168:171], v[176:179], v[106:109]
	v_mfma_f32_16x16x32_bf16 v[94:97], v[160:163], v[184:187], v[94:97]
	v_mfma_f32_16x16x32_bf16 v[90:93], v[168:171], v[184:187], v[90:93]
	v_mfma_f32_16x16x32_bf16 v[78:81], v[160:163], v[192:195], v[78:81]
	v_mfma_f32_16x16x32_bf16 v[74:77], v[168:171], v[192:195], v[74:77]
	v_mfma_f32_16x16x32_bf16 v[70:73], v[160:163], v[200:203], v[70:73]
	v_mfma_f32_16x16x32_bf16 v[66:69], v[168:171], v[200:203], v[66:69]
	v_mfma_f32_16x16x32_bf16 v[110:113], v[164:167], v[180:183], v[110:113]
	v_mfma_f32_16x16x32_bf16 v[106:109], v[172:175], v[180:183], v[106:109]
	v_mfma_f32_16x16x32_bf16 v[94:97], v[164:167], v[188:191], v[94:97]
	v_mfma_f32_16x16x32_bf16 v[90:93], v[172:175], v[188:191], v[90:93]
	v_mfma_f32_16x16x32_bf16 v[78:81], v[164:167], v[196:199], v[78:81]
	v_mfma_f32_16x16x32_bf16 v[74:77], v[172:175], v[196:199], v[74:77]
	v_mfma_f32_16x16x32_bf16 v[70:73], v[164:167], v[204:207], v[70:73]
	v_mfma_f32_16x16x32_bf16 v[66:69], v[172:175], v[204:207], v[66:69]
	s_setprio 0
	s_barrier
; #define PG8_STAGE_A(bufoff, kt, h, usenext) do { if constexpr (Sched::GATHER) { unsigned vo_[2] = { (usenext) ? goffN[h][0] : goff[h][0], (usenext) ? goffN[h][1] : goff[h][1] }; PG8_STAGE(bufoff, kt, vo_); } \
;         else { PG8_STAGE(bufoff, (kt) + ((h) ? hstep : 0), voffA); } } while (0)
; #define PG8_STAGE(bufoff, gbase, voff) do { _Pragma("unroll") for (int _i = 0; _i < 2; ++_i) \
;         __builtin_amdgcn_global_load_lds((const unsigned*)((const char*)(gbase) + (voff)[_i]), (LAS unsigned*)(lds + (bufoff) + ldsw + _i * 8192), 16, 0, 0); } while (0)
; template <class Epi, class Sched, bool ALIGN_EPI = true, bool SP2 = true>
; __device__ __forceinline__ void gemm_phase(LAS unsigned char* lds, const Gemm g, const Sched& S, const Epi& E, int tid_in) {
;     ...
;             PG8_LDA(At, 1, 1); PG8_STAGE(PG8_SB(1, 0), b3, voffB); PG8_STAGE(PG8_SB(1, 1), b3 + hstepB, voffB); PG8_STAGE_A(PG8_SA(1, 0), a3, 0, last);
;             PG8_WAIT_V(8); PG8_WAIT_L(0); PG8_BAR; PG8_MMA(1, 0, At, B0); PG8_MMA(1, 1, At, B1); PG8_BAR; PG8_SCHED;
;             } else {
;             PG8_LDB(B0, 0, 0); PG8_SCHED; PG8_LDA(At, 0, 0); PG8_STAGE_A(PG8_SA(1, 1), a1, 1, false);
;             PG8_WAIT_L(8); PG8_BAR; PG8_WAIT_L(0); PG8_MMA(0, 0, At, B0); PG8_BAR; PG8_SCHED;
;             PG8_LDB(B1, 0, 1); PG8_STAGE(PG8_SB(0, 0), b2, voffB);
;             PG8_BAR; PG8_WAIT_L(0); PG8_MMA(0, 1, At, B1); PG8_BAR;
;             PG8_LDA(At, 0, 1); PG8_STAGE_A(PG8_SA(0, 0), a2, 0, last);
;             PG8_BAR; PG8_WAIT_L(0); PG8_MMA(1, 0, At, B0); PG8_BAR; PG8_SCHED;
;             PG8_STAGE(PG8_SB(0, 1), b2 + hstepB, voffB);
;             PG8_WAIT_V(6); PG8_BAR; PG8_MMA(1, 1, At, B1); PG8_BAR;
;             PG8_LDB(B0, 1, 0); PG8_SCHED; PG8_LDA(At, 1, 0); PG8_STAGE_A(PG8_SA(0, 1), a2, 1, last);
;             PG8_WAIT_L(8); PG8_BAR; PG8_WAIT_L(0); PG8_MMA(0, 0, At, B0); PG8_BAR; PG8_SCHED;
;             PG8_LDB(B1, 1, 1); PG8_STAGE(PG8_SB(1, 0), b3, voffB);
;             PG8_BAR; PG8_WAIT_L(0); PG8_MMA(0, 1, At, B1); PG8_BAR;
;             PG8_LDA(At, 1, 1); PG8_STAGE_A(PG8_SA(1, 0), a3, 0, last);
;             PG8_BAR; PG8_WAIT_L(0); PG8_MMA(1, 0, At, B0); PG8_BAR; PG8_SCHED;
;             PG8_STAGE(PG8_SB(1, 1), b3 + hstepB, voffB);
;             PG8_WAIT_V(6); PG8_BAR; PG8_MMA(1, 1, At, B1); PG8_BAR;
;             }
;         }
;         if constexpr (ALIGN_EPI) { if (wr == 0) PG8_BAR; }
	s_mov_b32 m0, s41
	v_lshl_add_u64 v[208:209], v[208:209], 0, s[58:59]
	s_add_u32 s20, s20, 0x40080
	ds_read_b128 v[176:179], v143 offset:49152
	ds_read_b128 v[180:183], v143 offset:50176
	ds_read_b128 v[184:187], v143 offset:51200
	ds_read_b128 v[188:191], v143 offset:52224
	ds_read_b128 v[192:195], v143 offset:53248
	ds_read_b128 v[196:199], v143 offset:54272
	ds_read_b128 v[200:203], v143 offset:55296
	ds_read_b128 v[204:207], v143 offset:56320
	global_load_lds_dwordx4 v[208:209], off
	v_lshl_add_u64 v[208:209], v[210:211], 0, s[58:59]
	s_mov_b32 m0, s42
	s_addc_u32 s21, s21, 0
	global_load_lds_dwordx4 v[208:209], off
	v_lshl_add_u64 v[208:209], s[20:21], 0, v[64:65]
	s_mov_b32 m0, s47
	s_nop 0
	global_load_lds_dwordx4 v[208:209], off
	v_lshl_add_u64 v[208:209], s[20:21], 0, v[130:131]
	s_mov_b32 m0, s48
	s_nop 0
	global_load_lds_dwordx4 v[208:209], off
	v_lshl_add_u64 v[208:209], v[212:213], 0, s[58:59]
	s_mov_b32 m0, s43
	s_nop 0
	global_load_lds_dwordx4 v[208:209], off
	v_lshl_add_u64 v[208:209], v[214:215], 0, s[58:59]
	s_mov_b32 m0, s46
	s_nop 0
	global_load_lds_dwordx4 v[208:209], off
	s_waitcnt vmcnt(8)
	s_waitcnt lgkmcnt(0)
	s_barrier
	s_setprio 1
	s_waitcnt lgkmcnt(0)
	v_mfma_f32_16x16x32_bf16 v[60:63], v[144:147], v[176:179], v[60:63]
	v_mfma_f32_16x16x32_bf16 v[56:59], v[152:155], v[176:179], v[56:59]
	v_mfma_f32_16x16x32_bf16 v[52:55], v[144:147], v[184:187], v[52:55]
	v_mfma_f32_16x16x32_bf16 v[48:51], v[152:155], v[184:187], v[48:51]
	v_mfma_f32_16x16x32_bf16 v[36:39], v[144:147], v[192:195], v[36:39]
	v_mfma_f32_16x16x32_bf16 v[32:35], v[152:155], v[192:195], v[32:35]
	v_mfma_f32_16x16x32_bf16 v[20:23], v[144:147], v[200:203], v[20:23]
	v_mfma_f32_16x16x32_bf16 v[16:19], v[152:155], v[200:203], v[16:19]
	v_mfma_f32_16x16x32_bf16 v[60:63], v[148:151], v[180:183], v[60:63]
	v_mfma_f32_16x16x32_bf16 v[56:59], v[156:159], v[180:183], v[56:59]
	v_mfma_f32_16x16x32_bf16 v[52:55], v[148:151], v[188:191], v[52:55]
	v_mfma_f32_16x16x32_bf16 v[48:51], v[156:159], v[188:191], v[48:51]
	v_mfma_f32_16x16x32_bf16 v[36:39], v[148:151], v[196:199], v[36:39]
	v_mfma_f32_16x16x32_bf16 v[32:35], v[156:159], v[196:199], v[32:35]
	v_mfma_f32_16x16x32_bf16 v[20:23], v[148:151], v[204:207], v[20:23]
	v_mfma_f32_16x16x32_bf16 v[16:19], v[156:159], v[204:207], v[16:19]
	s_setprio 0
	s_setprio 1
	v_mfma_f32_16x16x32_bf16 v[44:47], v[160:163], v[176:179], v[44:47]
	v_mfma_f32_16x16x32_bf16 v[40:43], v[168:171], v[176:179], v[40:43]
	v_mfma_f32_16x16x32_bf16 v[28:31], v[160:163], v[184:187], v[28:31]
	v_mfma_f32_16x16x32_bf16 v[24:27], v[168:171], v[184:187], v[24:27]
	v_mfma_f32_16x16x32_bf16 v[12:15], v[160:163], v[192:195], v[12:15]
	v_mfma_f32_16x16x32_bf16 v[8:11], v[168:171], v[192:195], v[8:11]
	v_mfma_f32_16x16x32_bf16 v[4:7], v[160:163], v[200:203], v[4:7]
	v_mfma_f32_16x16x32_bf16 v[0:3], v[168:171], v[200:203], v[0:3]
	v_mfma_f32_16x16x32_bf16 v[44:47], v[164:167], v[180:183], v[44:47]
	v_mfma_f32_16x16x32_bf16 v[40:43], v[172:175], v[180:183], v[40:43]
	v_mfma_f32_16x16x32_bf16 v[28:31], v[164:167], v[188:191], v[28:31]
	v_mfma_f32_16x16x32_bf16 v[24:27], v[172:175], v[188:191], v[24:27]
	v_mfma_f32_16x16x32_bf16 v[12:15], v[164:167], v[196:199], v[12:15]
	v_mfma_f32_16x16x32_bf16 v[8:11], v[172:175], v[196:199], v[8:11]
	v_mfma_f32_16x16x32_bf16 v[4:7], v[164:167], v[204:207], v[4:7]
	v_mfma_f32_16x16x32_bf16 v[0:3], v[172:175], v[204:207], v[0:3]
	s_setprio 0
	s_add_i32 s55, s55, 2
	s_add_u32 s18, s18, 0x100
	s_addc_u32 s19, s19, 0
	s_add_u32 s53, s53, 0x100
	s_addc_u32 s54, s54, 0
	s_cmp_gt_u32 s55, 13
	s_barrier
	s_cbranch_scc0 .LBB0_717
	s_and_b64 vcc, exec, s[6:7]
	s_cbranch_vccz .LBB0_720
	s_barrier

; #define PG8_STAGE_A(bufoff, kt, h, usenext) do { if constexpr (Sched::GATHER) { unsigned vo_[2] = { (usenext) ? goffN[h][0] : goff[h][0], (usenext) ? goffN[h][1] : goff[h][1] }; PG8_STAGE(bufoff, kt, vo_); } \
;         else { PG8_STAGE(bufoff, (kt) + ((h) ? hstep : 0), voffA); } } while (0)
; #define PG8_STAGE(bufoff, gbase, voff) do { _Pragma("unroll") for (int _i = 0; _i < 2; ++_i) \
;         __builtin_amdgcn_global_load_lds((const unsigned*)((const char*)(gbase) + (voff)[_i]), (LAS unsigned*)(lds + (bufoff) + ldsw + _i * 8192), 16, 0, 0); } while (0)
; #define PG8_LDA(dst, b, h) do { _Pragma("unroll") for (int m = 0; m < 4; ++m) _Pragma("unroll") for (int k = 0; k < 2; ++k) dst[m][k] = *(const LAS bf16x8*)(lds + PG8_SA(b, h) + aoff + m * 2048 + k * 1024); } while (0)
; #define PG8_LDB(dst, b, h) do { _Pragma("unroll") for (int n = 0; n < 2; ++n) _Pragma("unroll") for (int k = 0; k < 2; ++k) dst[n][k] = *(const LAS bf16x8*)(lds + PG8_SB(b, h) + boff + n * 2048 + k * 1024); } while (0)
; #define PG8_MMA(ai, bj, At, Bt) do { __builtin_amdgcn_s_setprio(1); _Pragma("unroll") for (int m = 0; m < 4; ++m) _Pragma("unroll") for (int n = 0; n < 2; ++n) _Pragma("unroll") for (int k = 0; k < 2; ++k) \
;         acc[ai][bj][m][n] = __builtin_amdgcn_mfma_f32_16x16x32_bf16(Bt[n][k], At[m][k], acc[ai][bj][m][n], 0, 0, 0); __builtin_amdgcn_s_setprio(0); } while (0)
; #define PG8_WAIT_V(n) asm volatile("s_waitcnt vmcnt(" #n ")" ::: "memory")
; template <class Epi, class Sched, bool ALIGN_EPI = true, bool SP2 = true>
; __device__ __forceinline__ void gemm_phase(LAS unsigned char* lds, const Gemm g, const Sched& S, const Epi& E, int tid_in) {
;     ...
;             const char* a1 = cA + (size_t)(t + 1) * kstep;
;             const char* a2 = last ? nA : cA + (size_t)(t + 2) * kstep; const char* b2 = last ? nB : cB + (size_t)(t + 2) * kstep;
;             const char* a3 = a2 + kstep; const char* b3 = b2 + kstep;
;             if constexpr (SP2) {
;             PG8_LDB(B0, 0, 0); PG8_LDB(B1, 0, 1); PG8_SCHED; PG8_LDA(At, 0, 0); PG8_STAGE_A(PG8_SA(1, 1), a1, 1, false);
;             PG8_WAIT_V(8); PG8_WAIT_L(0); PG8_BAR; PG8_MMA(0, 0, At, B0); PG8_MMA(0, 1, At, B1); PG8_BAR; PG8_SCHED;
;             PG8_LDA(At, 0, 1); PG8_STAGE(PG8_SB(0, 0), b2, voffB); PG8_STAGE(PG8_SB(0, 1), b2 + hstepB, voffB); PG8_STAGE_A(PG8_SA(0, 0), a2, 0, last);
.LBB0_1337:
	v_add_u32_e32 v142, s33, v167
	v_add_u32_e32 v166, s36, v167
	ds_read_b128 v[130:133], v142
	ds_read_b128 v[134:137], v142 offset:1024
	ds_read_b128 v[138:141], v142 offset:2048
	ds_read_b128 v[142:145], v142 offset:3072
	ds_read_b128 v[158:161], v166
	ds_read_b128 v[162:165], v166 offset:1024
	ds_read_b128 v[176:179], v166 offset:2048
	ds_read_b128 v[180:183], v166 offset:3072
	s_add_u32 s30, s28, 0xfffc0080
	s_addc_u32 s31, s29, -1
	s_cmp_eq_u32 s64, 12
	s_cselect_b32 s35, s21, s31
	s_cselect_b32 s34, s44, s30
	s_cselect_b32 s31, s19, s63
	s_cselect_b32 s30, s61, s62
	v_lshl_add_u64 v[216:217], s[28:29], 0, v[154:155]
	s_add_i32 m0, s42, 0xc000
	ds_read_b128 v[184:187], v174
	ds_read_b128 v[188:191], v174 offset:1024
	ds_read_b128 v[192:195], v174 offset:2048
	ds_read_b128 v[196:199], v174 offset:3072
	ds_read_b128 v[200:203], v174 offset:4096
	ds_read_b128 v[204:207], v174 offset:5120
	ds_read_b128 v[208:211], v174 offset:6144
	ds_read_b128 v[212:215], v174 offset:7168
	global_load_lds_dwordx4 v[216:217], off
	v_lshl_add_u64 v[216:217], s[28:29], 0, v[156:157]
	s_add_i32 m0, s42, 0xe000
	s_nop 0
	global_load_lds_dwordx4 v[216:217], off
	s_waitcnt vmcnt(8)
	s_waitcnt lgkmcnt(0)
	s_barrier
	s_setprio 1
	s_waitcnt lgkmcnt(0)
	v_mfma_f32_16x16x32_bf16 v[126:129], v[130:133], v[184:187], v[126:129]
	v_mfma_f32_16x16x32_bf16 v[122:125], v[138:141], v[184:187], v[122:125]
	v_mfma_f32_16x16x32_bf16 v[118:121], v[130:133], v[192:195], v[118:121]
	v_mfma_f32_16x16x32_bf16 v[114:117], v[138:141], v[192:195], v[114:117]
	v_mfma_f32_16x16x32_bf16 v[102:105], v[130:133], v[200:203], v[102:105]
	v_mfma_f32_16x16x32_bf16 v[98:101], v[138:141], v[200:203], v[98:101]
	v_mfma_f32_16x16x32_bf16 v[86:89], v[130:133], v[208:211], v[86:89]
	v_mfma_f32_16x16x32_bf16 v[82:85], v[138:141], v[208:211], v[82:85]
	v_mfma_f32_16x16x32_bf16 v[126:129], v[134:137], v[188:191], v[126:129]
	v_mfma_f32_16x16x32_bf16 v[122:125], v[142:145], v[188:191], v[122:125]
	v_mfma_f32_16x16x32_bf16 v[118:121], v[134:137], v[196:199], v[118:121]
	v_mfma_f32_16x16x32_bf16 v[114:117], v[142:145], v[196:199], v[114:117]
	v_mfma_f32_16x16x32_bf16 v[102:105], v[134:137], v[204:207], v[102:105]
	v_mfma_f32_16x16x32_bf16 v[98:101], v[142:145], v[204:207], v[98:101]
	v_mfma_f32_16x16x32_bf16 v[86:89], v[134:137], v[212:215], v[86:89]
	v_mfma_f32_16x16x32_bf16 v[82:85], v[142:145], v[212:215], v[82:85]
	s_setprio 0
	s_setprio 1
	v_mfma_f32_16x16x32_bf16 v[110:113], v[158:161], v[184:187], v[110:113]
	v_mfma_f32_16x16x32_bf16 v[106:109], v[176:179], v[184:187], v[106:109]
	v_mfma_f32_16x16x32_bf16 v[94:97], v[158:161], v[192:195], v[94:97]
	v_mfma_f32_16x16x32_bf16 v[90:93], v[176:179], v[192:195], v[90:93]
	v_mfma_f32_16x16x32_bf16 v[78:81], v[158:161], v[200:203], v[78:81]
	v_mfma_f32_16x16x32_bf16 v[74:77], v[176:179], v[200:203], v[74:77]
	v_mfma_f32_16x16x32_bf16 v[70:73], v[158:161], v[208:211], v[70:73]
	v_mfma_f32_16x16x32_bf16 v[66:69], v[176:179], v[208:211], v[66:69]
	v_mfma_f32_16x16x32_bf16 v[110:113], v[162:165], v[188:191], v[110:113]
	v_mfma_f32_16x16x32_bf16 v[106:109], v[180:183], v[188:191], v[106:109]
	v_mfma_f32_16x16x32_bf16 v[94:97], v[162:165], v[196:199], v[94:97]
	v_mfma_f32_16x16x32_bf16 v[90:93], v[180:183], v[196:199], v[90:93]
	v_mfma_f32_16x16x32_bf16 v[78:81], v[162:165], v[204:207], v[78:81]
	v_mfma_f32_16x16x32_bf16 v[74:77], v[180:183], v[204:207], v[74:77]
	v_mfma_f32_16x16x32_bf16 v[70:73], v[162:165], v[212:215], v[70:73]
	v_mfma_f32_16x16x32_bf16 v[66:69], v[180:183], v[212:215], v[66:69]
	s_setprio 0
	s_barrier
	s_mov_b32 m0, s38
	v_lshl_add_u64 v[216:217], s[30:31], 0, v[64:65]
	s_add_u32 s66, s30, 0x10000
	ds_read_b128 v[184:187], v174 offset:16384
	ds_read_b128 v[188:191], v174 offset:17408
	ds_read_b128 v[192:195], v174 offset:18432
	ds_read_b128 v[196:199], v174 offset:19456
	ds_read_b128 v[200:203], v174 offset:20480
	ds_read_b128 v[204:207], v174 offset:21504
	ds_read_b128 v[208:211], v174 offset:22528
	ds_read_b128 v[212:215], v174 offset:23552
	global_load_lds_dwordx4 v[216:217], off
	v_lshl_add_u64 v[218:219], s[30:31], 0, v[146:147]
	s_mov_b32 m0, s39
	s_addc_u32 s67, s31, 0
	global_load_lds_dwordx4 v[218:219], off
	v_lshl_add_u64 v[220:221], s[66:67], 0, v[64:65]
	s_mov_b32 m0, s40
	v_lshl_add_u64 v[222:223], s[34:35], 0, v[148:149]
	global_load_lds_dwordx4 v[220:221], off
	v_lshl_add_u64 v[220:221], s[66:67], 0, v[146:147]
	s_mov_b32 m0, s41
	s_nop 0
	global_load_lds_dwordx4 v[220:221], off
	v_lshl_add_u64 v[220:221], s[34:35], 0, v[150:151]
	s_mov_b32 m0, s42
	s_nop 0
	global_load_lds_dwordx4 v[220:221], off
	s_mov_b32 m0, s43
	s_nop 0
	global_load_lds_dwordx4 v[222:223], off
	s_waitcnt vmcnt(8)
	s_waitcnt lgkmcnt(0)
	s_barrier
; #define PG8_STAGE_A(bufoff, kt, h, usenext) do { if constexpr (Sched::GATHER) { unsigned vo_[2] = { (usenext) ? goffN[h][0] : goff[h][0], (usenext) ? goffN[h][1] : goff[h][1] }; PG8_STAGE(bufoff, kt, vo_); } \
;         else { PG8_STAGE(bufoff, (kt) + ((h) ? hstep : 0), voffA); } } while (0)
; #define PG8_LDA(dst, b, h) do { _Pragma("unroll") for (int m = 0; m < 4; ++m) _Pragma("unroll") for (int k = 0; k < 2; ++k) dst[m][k] = *(const LAS bf16x8*)(lds + PG8_SA(b, h) + aoff + m * 2048 + k * 1024); } while (0)
; #define PG8_LDB(dst, b, h) do { _Pragma("unroll") for (int n = 0; n < 2; ++n) _Pragma("unroll") for (int k = 0; k < 2; ++k) dst[n][k] = *(const LAS bf16x8*)(lds + PG8_SB(b, h) + boff + n * 2048 + k * 1024); } while (0)
; #define PG8_MMA(ai, bj, At, Bt) do { __builtin_amdgcn_s_setprio(1); _Pragma("unroll") for (int m = 0; m < 4; ++m) _Pragma("unroll") for (int n = 0; n < 2; ++n) _Pragma("unroll") for (int k = 0; k < 2; ++k) \
;         acc[ai][bj][m][n] = __builtin_amdgcn_mfma_f32_16x16x32_bf16(Bt[n][k], At[m][k], acc[ai][bj][m][n], 0, 0, 0); __builtin_amdgcn_s_setprio(0); } while (0)
; #define PG8_WAIT_V(n) asm volatile("s_waitcnt vmcnt(" #n ")" ::: "memory")
; #define PG8_WAIT_L(n) asm volatile("s_waitcnt lgkmcnt(" #n ")" ::: "memory")
; #define PG8_BAR __builtin_amdgcn_s_barrier()
; #define PG8_SCHED __builtin_amdgcn_sched_barrier(0)
; template <class Epi, class Sched, bool ALIGN_EPI = true, bool SP2 = true>
; __device__ __forceinline__ void gemm_phase(LAS unsigned char* lds, const Gemm g, const Sched& S, const Epi& E, int tid_in) {
;     ...
;             PG8_WAIT_V(8); PG8_WAIT_L(0); PG8_BAR; PG8_MMA(1, 0, At, B0); PG8_MMA(1, 1, At, B1); PG8_BAR; PG8_SCHED;
;             PG8_LDB(B0, 1, 0); PG8_LDB(B1, 1, 1); PG8_SCHED; PG8_LDA(At, 1, 0); PG8_STAGE_A(PG8_SA(0, 1), a2, 1, last);
;             PG8_WAIT_V(8); PG8_WAIT_L(0); PG8_BAR; PG8_MMA(0, 0, At, B0); PG8_MMA(0, 1, At, B1); PG8_BAR; PG8_SCHED;
	s_setprio 1
	s_waitcnt lgkmcnt(0)
	v_mfma_f32_16x16x32_bf16 v[60:63], v[130:133], v[184:187], v[60:63]
	v_mfma_f32_16x16x32_bf16 v[56:59], v[138:141], v[184:187], v[56:59]
	v_mfma_f32_16x16x32_bf16 v[52:55], v[130:133], v[192:195], v[52:55]
	v_mfma_f32_16x16x32_bf16 v[48:51], v[138:141], v[192:195], v[48:51]
	v_mfma_f32_16x16x32_bf16 v[36:39], v[130:133], v[200:203], v[36:39]
	v_mfma_f32_16x16x32_bf16 v[32:35], v[138:141], v[200:203], v[32:35]
	v_mfma_f32_16x16x32_bf16 v[20:23], v[130:133], v[208:211], v[20:23]
	v_mfma_f32_16x16x32_bf16 v[16:19], v[138:141], v[208:211], v[16:19]
	v_mfma_f32_16x16x32_bf16 v[60:63], v[134:137], v[188:191], v[60:63]
	v_mfma_f32_16x16x32_bf16 v[56:59], v[142:145], v[188:191], v[56:59]
	v_mfma_f32_16x16x32_bf16 v[52:55], v[134:137], v[196:199], v[52:55]
	v_mfma_f32_16x16x32_bf16 v[48:51], v[142:145], v[196:199], v[48:51]
	v_mfma_f32_16x16x32_bf16 v[36:39], v[134:137], v[204:207], v[36:39]
	v_mfma_f32_16x16x32_bf16 v[32:35], v[142:145], v[204:207], v[32:35]
	v_mfma_f32_16x16x32_bf16 v[20:23], v[134:137], v[212:215], v[20:23]
	v_mfma_f32_16x16x32_bf16 v[16:19], v[142:145], v[212:215], v[16:19]
	s_setprio 0
	s_setprio 1
	v_mfma_f32_16x16x32_bf16 v[44:47], v[158:161], v[184:187], v[44:47]
	v_mfma_f32_16x16x32_bf16 v[40:43], v[176:179], v[184:187], v[40:43]
	v_mfma_f32_16x16x32_bf16 v[28:31], v[158:161], v[192:195], v[28:31]
	v_mfma_f32_16x16x32_bf16 v[24:27], v[176:179], v[192:195], v[24:27]
	v_mfma_f32_16x16x32_bf16 v[12:15], v[158:161], v[200:203], v[12:15]
	v_mfma_f32_16x16x32_bf16 v[8:11], v[176:179], v[200:203], v[8:11]
	v_mfma_f32_16x16x32_bf16 v[4:7], v[158:161], v[208:211], v[4:7]
	v_mfma_f32_16x16x32_bf16 v[0:3], v[176:179], v[208:211], v[0:3]
	v_mfma_f32_16x16x32_bf16 v[44:47], v[162:165], v[188:191], v[44:47]
	v_mfma_f32_16x16x32_bf16 v[40:43], v[180:183], v[188:191], v[40:43]
	v_mfma_f32_16x16x32_bf16 v[28:31], v[162:165], v[196:199], v[28:31]
	v_mfma_f32_16x16x32_bf16 v[24:27], v[180:183], v[196:199], v[24:27]
	v_mfma_f32_16x16x32_bf16 v[12:15], v[162:165], v[204:207], v[12:15]
	v_mfma_f32_16x16x32_bf16 v[8:11], v[180:183], v[204:207], v[8:11]
	v_mfma_f32_16x16x32_bf16 v[4:7], v[162:165], v[212:215], v[4:7]
	v_mfma_f32_16x16x32_bf16 v[0:3], v[180:183], v[212:215], v[0:3]
	s_setprio 0
	s_barrier
	v_add_u32_e32 v142, s48, v167
	v_add_u32_e32 v166, s49, v167
	ds_read_b128 v[130:133], v142
	ds_read_b128 v[134:137], v142 offset:1024
	ds_read_b128 v[138:141], v142 offset:2048
	ds_read_b128 v[142:145], v142 offset:3072
	ds_read_b128 v[158:161], v166
	ds_read_b128 v[162:165], v166 offset:1024
	ds_read_b128 v[176:179], v166 offset:2048
	ds_read_b128 v[180:183], v166 offset:3072
	s_add_u32 s34, s34, 0x40000
	s_addc_u32 s35, s35, 0
	s_mov_b32 m0, s46
	v_lshl_add_u64 v[226:227], s[34:35], 0, v[150:151]
	ds_read_b128 v[184:187], v174 offset:32768
	ds_read_b128 v[188:191], v174 offset:33792
	ds_read_b128 v[192:195], v174 offset:34816
	ds_read_b128 v[196:199], v174 offset:35840
	ds_read_b128 v[200:203], v174 offset:36864
	ds_read_b128 v[204:207], v174 offset:37888
	ds_read_b128 v[208:211], v174 offset:38912
	ds_read_b128 v[212:215], v174 offset:39936
	global_load_lds_dwordx4 v[226:227], off
	v_lshl_add_u64 v[226:227], s[34:35], 0, v[148:149]
	s_mov_b32 m0, s47
	s_nop 0
	global_load_lds_dwordx4 v[226:227], off
	s_waitcnt vmcnt(8)
	s_waitcnt lgkmcnt(0)
	s_barrier
	s_setprio 1
	s_waitcnt lgkmcnt(0)
	v_mfma_f32_16x16x32_bf16 v[126:129], v[130:133], v[184:187], v[126:129]
	v_mfma_f32_16x16x32_bf16 v[122:125], v[138:141], v[184:187], v[122:125]
	v_mfma_f32_16x16x32_bf16 v[118:121], v[130:133], v[192:195], v[118:121]
	v_mfma_f32_16x16x32_bf16 v[114:117], v[138:141], v[192:195], v[114:117]
	v_mfma_f32_16x16x32_bf16 v[102:105], v[130:133], v[200:203], v[102:105]
	v_mfma_f32_16x16x32_bf16 v[98:101], v[138:141], v[200:203], v[98:101]
	v_mfma_f32_16x16x32_bf16 v[86:89], v[130:133], v[208:211], v[86:89]
	v_mfma_f32_16x16x32_bf16 v[82:85], v[138:141], v[208:211], v[82:85]
	v_mfma_f32_16x16x32_bf16 v[126:129], v[134:137], v[188:191], v[126:129]
	v_mfma_f32_16x16x32_bf16 v[122:125], v[142:145], v[188:191], v[122:125]
	v_mfma_f32_16x16x32_bf16 v[118:121], v[134:137], v[196:199], v[118:121]
	v_mfma_f32_16x16x32_bf16 v[114:117], v[142:145], v[196:199], v[114:117]
	v_mfma_f32_16x16x32_bf16 v[102:105], v[134:137], v[204:207], v[102:105]
	v_mfma_f32_16x16x32_bf16 v[98:101], v[142:145], v[204:207], v[98:101]
	v_mfma_f32_16x16x32_bf16 v[86:89], v[134:137], v[212:215], v[86:89]
	v_mfma_f32_16x16x32_bf16 v[82:85], v[142:145], v[212:215], v[82:85]
	s_setprio 0
	s_setprio 1
	v_mfma_f32_16x16x32_bf16 v[110:113], v[158:161], v[184:187], v[110:113]
	v_mfma_f32_16x16x32_bf16 v[106:109], v[176:179], v[184:187], v[106:109]
	v_mfma_f32_16x16x32_bf16 v[94:97], v[158:161], v[192:195], v[94:97]
	v_mfma_f32_16x16x32_bf16 v[90:93], v[176:179], v[192:195], v[90:93]
	v_mfma_f32_16x16x32_bf16 v[78:81], v[158:161], v[200:203], v[78:81]
	v_mfma_f32_16x16x32_bf16 v[74:77], v[176:179], v[200:203], v[74:77]
	v_mfma_f32_16x16x32_bf16 v[70:73], v[158:161], v[208:211], v[70:73]
	v_mfma_f32_16x16x32_bf16 v[66:69], v[176:179], v[208:211], v[66:69]
	v_mfma_f32_16x16x32_bf16 v[110:113], v[162:165], v[188:191], v[110:113]
	v_mfma_f32_16x16x32_bf16 v[106:109], v[180:183], v[188:191], v[106:109]
	v_mfma_f32_16x16x32_bf16 v[94:97], v[162:165], v[196:199], v[94:97]
	v_mfma_f32_16x16x32_bf16 v[90:93], v[180:183], v[196:199], v[90:93]
	v_mfma_f32_16x16x32_bf16 v[78:81], v[162:165], v[204:207], v[78:81]
	v_mfma_f32_16x16x32_bf16 v[74:77], v[180:183], v[204:207], v[74:77]
	v_mfma_f32_16x16x32_bf16 v[70:73], v[162:165], v[212:215], v[70:73]
	v_mfma_f32_16x16x32_bf16 v[66:69], v[180:183], v[212:215], v[66:69]
	s_setprio 0
	s_barrier
; #define PG8_STAGE_A(bufoff, kt, h, usenext) do { if constexpr (Sched::GATHER) { unsigned vo_[2] = { (usenext) ? goffN[h][0] : goff[h][0], (usenext) ? goffN[h][1] : goff[h][1] }; PG8_STAGE(bufoff, kt, vo_); } \
;         else { PG8_STAGE(bufoff, (kt) + ((h) ? hstep : 0), voffA); } } while (0)
; #define PG8_STAGE(bufoff, gbase, voff) do { _Pragma("unroll") for (int _i = 0; _i < 2; ++_i) \
;         __builtin_amdgcn_global_load_lds((const unsigned*)((const char*)(gbase) + (voff)[_i]), (LAS unsigned*)(lds + (bufoff) + ldsw + _i * 8192), 16, 0, 0); } while (0)
; template <class Epi, class Sched, bool ALIGN_EPI = true, bool SP2 = true>
; __device__ __forceinline__ void gemm_phase(LAS unsigned char* lds, const Gemm g, const Sched& S, const Epi& E, int tid_in) {
;     ...
;             PG8_LDA(At, 1, 1); PG8_STAGE(PG8_SB(1, 0), b3, voffB); PG8_STAGE(PG8_SB(1, 1), b3 + hstepB, voffB); PG8_STAGE_A(PG8_SA(1, 0), a3, 0, last);
;             PG8_WAIT_V(8); PG8_WAIT_L(0); PG8_BAR; PG8_MMA(1, 0, At, B0); PG8_MMA(1, 1, At, B1); PG8_BAR; PG8_SCHED;
;             } else {
;             PG8_LDB(B0, 0, 0); PG8_SCHED; PG8_LDA(At, 0, 0); PG8_STAGE_A(PG8_SA(1, 1), a1, 1, false);
;             PG8_WAIT_L(8); PG8_BAR; PG8_WAIT_L(0); PG8_MMA(0, 0, At, B0); PG8_BAR; PG8_SCHED;
;             PG8_LDB(B1, 0, 1); PG8_STAGE(PG8_SB(0, 0), b2, voffB);
;             PG8_BAR; PG8_WAIT_L(0); PG8_MMA(0, 1, At, B1); PG8_BAR;
;             PG8_LDA(At, 0, 1); PG8_STAGE_A(PG8_SA(0, 0), a2, 0, last);
;             PG8_BAR; PG8_WAIT_L(0); PG8_MMA(1, 0, At, B0); PG8_BAR; PG8_SCHED;
;             PG8_STAGE(PG8_SB(0, 1), b2 + hstepB, voffB);
;             PG8_WAIT_V(6); PG8_BAR; PG8_MMA(1, 1, At, B1); PG8_BAR;
;             PG8_LDB(B0, 1, 0); PG8_SCHED; PG8_LDA(At, 1, 0); PG8_STAGE_A(PG8_SA(0, 1), a2, 1, last);
;             PG8_WAIT_L(8); PG8_BAR; PG8_WAIT_L(0); PG8_MMA(0, 0, At, B0); PG8_BAR; PG8_SCHED;
;             PG8_LDB(B1, 1, 1); PG8_STAGE(PG8_SB(1, 0), b3, voffB);
;             PG8_BAR; PG8_WAIT_L(0); PG8_MMA(0, 1, At, B1); PG8_BAR;
;             PG8_LDA(At, 1, 1); PG8_STAGE_A(PG8_SA(1, 0), a3, 0, last);
;             PG8_BAR; PG8_WAIT_L(0); PG8_MMA(1, 0, At, B0); PG8_BAR; PG8_SCHED;
;             PG8_STAGE(PG8_SB(1, 1), b3 + hstepB, voffB);
;             PG8_WAIT_V(6); PG8_BAR; PG8_MMA(1, 1, At, B1); PG8_BAR;
;             }
;         }
;         if constexpr (ALIGN_EPI) { if (wr == 0) PG8_BAR; }
	s_mov_b32 m0, s51
	v_lshl_add_u64 v[216:217], v[216:217], 0, s[70:71]
	s_add_u32 s30, s30, 0x10080
	ds_read_b128 v[184:187], v174 offset:49152
	ds_read_b128 v[188:191], v174 offset:50176
	ds_read_b128 v[192:195], v174 offset:51200
	ds_read_b128 v[196:199], v174 offset:52224
	ds_read_b128 v[200:203], v174 offset:53248
	ds_read_b128 v[204:207], v174 offset:54272
	ds_read_b128 v[208:211], v174 offset:55296
	ds_read_b128 v[212:215], v174 offset:56320
	global_load_lds_dwordx4 v[216:217], off
	v_lshl_add_u64 v[216:217], v[218:219], 0, s[70:71]
	s_mov_b32 m0, s52
	s_addc_u32 s31, s31, 0
	global_load_lds_dwordx4 v[216:217], off
	v_lshl_add_u64 v[216:217], s[30:31], 0, v[64:65]
	s_mov_b32 m0, s55
	s_nop 0
	global_load_lds_dwordx4 v[216:217], off
	v_lshl_add_u64 v[216:217], s[30:31], 0, v[146:147]
	s_mov_b32 m0, s56
	s_nop 0
	global_load_lds_dwordx4 v[216:217], off
	v_lshl_add_u64 v[216:217], v[220:221], 0, s[70:71]
	s_mov_b32 m0, s53
	s_nop 0
	global_load_lds_dwordx4 v[216:217], off
	v_lshl_add_u64 v[216:217], v[222:223], 0, s[70:71]
	s_mov_b32 m0, s54
	s_nop 0
	global_load_lds_dwordx4 v[216:217], off
	s_waitcnt vmcnt(8)
	s_waitcnt lgkmcnt(0)
	s_barrier
	s_setprio 1
	s_waitcnt lgkmcnt(0)
	v_mfma_f32_16x16x32_bf16 v[60:63], v[130:133], v[184:187], v[60:63]
	v_mfma_f32_16x16x32_bf16 v[56:59], v[138:141], v[184:187], v[56:59]
	v_mfma_f32_16x16x32_bf16 v[52:55], v[130:133], v[192:195], v[52:55]
	v_mfma_f32_16x16x32_bf16 v[48:51], v[138:141], v[192:195], v[48:51]
	v_mfma_f32_16x16x32_bf16 v[36:39], v[130:133], v[200:203], v[36:39]
	v_mfma_f32_16x16x32_bf16 v[32:35], v[138:141], v[200:203], v[32:35]
	v_mfma_f32_16x16x32_bf16 v[20:23], v[130:133], v[208:211], v[20:23]
	v_mfma_f32_16x16x32_bf16 v[16:19], v[138:141], v[208:211], v[16:19]
	v_mfma_f32_16x16x32_bf16 v[60:63], v[134:137], v[188:191], v[60:63]
	v_mfma_f32_16x16x32_bf16 v[56:59], v[142:145], v[188:191], v[56:59]
	v_mfma_f32_16x16x32_bf16 v[52:55], v[134:137], v[196:199], v[52:55]
	v_mfma_f32_16x16x32_bf16 v[48:51], v[142:145], v[196:199], v[48:51]
	v_mfma_f32_16x16x32_bf16 v[36:39], v[134:137], v[204:207], v[36:39]
	v_mfma_f32_16x16x32_bf16 v[32:35], v[142:145], v[204:207], v[32:35]
	v_mfma_f32_16x16x32_bf16 v[20:23], v[134:137], v[212:215], v[20:23]
	v_mfma_f32_16x16x32_bf16 v[16:19], v[142:145], v[212:215], v[16:19]
	s_setprio 0
	s_setprio 1
	v_mfma_f32_16x16x32_bf16 v[44:47], v[158:161], v[184:187], v[44:47]
	v_mfma_f32_16x16x32_bf16 v[40:43], v[176:179], v[184:187], v[40:43]
	v_mfma_f32_16x16x32_bf16 v[28:31], v[158:161], v[192:195], v[28:31]
	v_mfma_f32_16x16x32_bf16 v[24:27], v[176:179], v[192:195], v[24:27]
	v_mfma_f32_16x16x32_bf16 v[12:15], v[158:161], v[200:203], v[12:15]
	v_mfma_f32_16x16x32_bf16 v[8:11], v[176:179], v[200:203], v[8:11]
	v_mfma_f32_16x16x32_bf16 v[4:7], v[158:161], v[208:211], v[4:7]
	v_mfma_f32_16x16x32_bf16 v[0:3], v[176:179], v[208:211], v[0:3]
	v_mfma_f32_16x16x32_bf16 v[44:47], v[162:165], v[188:191], v[44:47]
	v_mfma_f32_16x16x32_bf16 v[40:43], v[180:183], v[188:191], v[40:43]
	v_mfma_f32_16x16x32_bf16 v[28:31], v[162:165], v[196:199], v[28:31]
	v_mfma_f32_16x16x32_bf16 v[24:27], v[180:183], v[196:199], v[24:27]
	v_mfma_f32_16x16x32_bf16 v[12:15], v[162:165], v[204:207], v[12:15]
	v_mfma_f32_16x16x32_bf16 v[8:11], v[180:183], v[204:207], v[8:11]
	v_mfma_f32_16x16x32_bf16 v[4:7], v[162:165], v[212:215], v[4:7]
	v_mfma_f32_16x16x32_bf16 v[0:3], v[180:183], v[212:215], v[0:3]
	s_setprio 0
	s_add_i32 s64, s64, 2
	s_add_u32 s28, s28, 0x100
	s_addc_u32 s29, s29, 0
	s_add_u32 s62, s62, 0x100
	s_addc_u32 s63, s63, 0
	s_cmp_gt_u32 s64, 13
	s_barrier
	s_cbranch_scc0 .LBB0_1337
	s_and_b64 vcc, exec, s[14:15]
	s_cbranch_vccz .LBB0_1340
	s_barrier

; #define PG8_STAGE_A(bufoff, kt, h, usenext) do { if constexpr (Sched::GATHER) { unsigned vo_[2] = { (usenext) ? goffN[h][0] : goff[h][0], (usenext) ? goffN[h][1] : goff[h][1] }; PG8_STAGE(bufoff, kt, vo_); } \
;         else { PG8_STAGE(bufoff, (kt) + ((h) ? hstep : 0), voffA); } } while (0)
; #define PG8_STAGE(bufoff, gbase, voff) do { _Pragma("unroll") for (int _i = 0; _i < 2; ++_i) \
;         __builtin_amdgcn_global_load_lds((const unsigned*)((const char*)(gbase) + (voff)[_i]), (LAS unsigned*)(lds + (bufoff) + ldsw + _i * 8192), 16, 0, 0); } while (0)
; #define PG8_LDA(dst, b, h) do { _Pragma("unroll") for (int m = 0; m < 4; ++m) _Pragma("unroll") for (int k = 0; k < 2; ++k) dst[m][k] = *(const LAS bf16x8*)(lds + PG8_SA(b, h) + aoff + m * 2048 + k * 1024); } while (0)
; #define PG8_LDB(dst, b, h) do { _Pragma("unroll") for (int n = 0; n < 2; ++n) _Pragma("unroll") for (int k = 0; k < 2; ++k) dst[n][k] = *(const LAS bf16x8*)(lds + PG8_SB(b, h) + boff + n * 2048 + k * 1024); } while (0)
; #define PG8_MMA(ai, bj, At, Bt) do { __builtin_amdgcn_s_setprio(1); _Pragma("unroll") for (int m = 0; m < 4; ++m) _Pragma("unroll") for (int n = 0; n < 2; ++n) _Pragma("unroll") for (int k = 0; k < 2; ++k) \
;         acc[ai][bj][m][n] = __builtin_amdgcn_mfma_f32_16x16x32_bf16(Bt[n][k], At[m][k], acc[ai][bj][m][n], 0, 0, 0); __builtin_amdgcn_s_setprio(0); } while (0)
; #define PG8_WAIT_V(n) asm volatile("s_waitcnt vmcnt(" #n ")" ::: "memory")
; template <class Epi, class Sched, bool ALIGN_EPI = true, bool SP2 = true>
; __device__ __forceinline__ void gemm_phase(LAS unsigned char* lds, const Gemm g, const Sched& S, const Epi& E, int tid_in) {
;     ...
;             const char* a1 = cA + (size_t)(t + 1) * kstep;
;             const char* a2 = last ? nA : cA + (size_t)(t + 2) * kstep; const char* b2 = last ? nB : cB + (size_t)(t + 2) * kstep;
;             const char* a3 = a2 + kstep; const char* b3 = b2 + kstep;
;             if constexpr (SP2) {
;             PG8_LDB(B0, 0, 0); PG8_LDB(B1, 0, 1); PG8_SCHED; PG8_LDA(At, 0, 0); PG8_STAGE_A(PG8_SA(1, 1), a1, 1, false);
;             PG8_WAIT_V(8); PG8_WAIT_L(0); PG8_BAR; PG8_MMA(0, 0, At, B0); PG8_MMA(0, 1, At, B1); PG8_BAR; PG8_SCHED;
;             PG8_LDA(At, 0, 1); PG8_STAGE(PG8_SB(0, 0), b2, voffB); PG8_STAGE(PG8_SB(0, 1), b2 + hstepB, voffB); PG8_STAGE_A(PG8_SA(0, 0), a2, 0, last);
.LBB0_2333:
	v_add_u32_e32 v140, s24, v143
	ds_read_b128 v[146:149], v140
	ds_read_b128 v[150:153], v140 offset:1024
	ds_read_b128 v[154:157], v140 offset:2048
	ds_read_b128 v[158:161], v140 offset:3072
	v_add_u32_e32 v140, s25, v143
	ds_read_b128 v[162:165], v140
	ds_read_b128 v[166:169], v140 offset:1024
	ds_read_b128 v[170:173], v140 offset:2048
	ds_read_b128 v[174:177], v140 offset:3072
	s_add_u32 s20, s18, 0xfffc0080
	s_addc_u32 s21, s19, -1
	s_cmp_eq_u32 s51, 12
	s_cselect_b32 s23, s11, s21
	s_cselect_b32 s22, s47, s20
	s_cselect_b32 s21, s9, s50
	s_cselect_b32 s20, s48, s49
	v_lshl_add_u64 v[140:141], s[18:19], 0, v[136:137]
	s_add_i32 m0, s30, 0xc000
	ds_read_b128 v[178:181], v145
	ds_read_b128 v[182:185], v145 offset:1024
	ds_read_b128 v[186:189], v145 offset:2048
	ds_read_b128 v[190:193], v145 offset:3072
	ds_read_b128 v[194:197], v145 offset:4096
	ds_read_b128 v[198:201], v145 offset:5120
	ds_read_b128 v[202:205], v145 offset:6144
	ds_read_b128 v[206:209], v145 offset:7168
	global_load_lds_dwordx4 v[140:141], off
	v_lshl_add_u64 v[140:141], s[18:19], 0, v[138:139]
	s_add_i32 m0, s30, 0xe000
	s_nop 0
	global_load_lds_dwordx4 v[140:141], off
	s_waitcnt vmcnt(8)
	s_waitcnt lgkmcnt(0)
	s_barrier
	s_setprio 1
	s_waitcnt lgkmcnt(0)
	v_mfma_f32_16x16x32_bf16 v[126:129], v[146:149], v[178:181], v[126:129]
	v_mfma_f32_16x16x32_bf16 v[122:125], v[154:157], v[178:181], v[122:125]
	v_mfma_f32_16x16x32_bf16 v[110:113], v[146:149], v[186:189], v[110:113]
	v_mfma_f32_16x16x32_bf16 v[106:109], v[154:157], v[186:189], v[106:109]
	v_mfma_f32_16x16x32_bf16 v[94:97], v[146:149], v[194:197], v[94:97]
	v_mfma_f32_16x16x32_bf16 v[90:93], v[154:157], v[194:197], v[90:93]
	v_mfma_f32_16x16x32_bf16 v[78:81], v[146:149], v[202:205], v[78:81]
	v_mfma_f32_16x16x32_bf16 v[74:77], v[154:157], v[202:205], v[74:77]
	v_mfma_f32_16x16x32_bf16 v[126:129], v[150:153], v[182:185], v[126:129]
	v_mfma_f32_16x16x32_bf16 v[122:125], v[158:161], v[182:185], v[122:125]
	v_mfma_f32_16x16x32_bf16 v[110:113], v[150:153], v[190:193], v[110:113]
	v_mfma_f32_16x16x32_bf16 v[106:109], v[158:161], v[190:193], v[106:109]
	v_mfma_f32_16x16x32_bf16 v[94:97], v[150:153], v[198:201], v[94:97]
	v_mfma_f32_16x16x32_bf16 v[90:93], v[158:161], v[198:201], v[90:93]
	v_mfma_f32_16x16x32_bf16 v[78:81], v[150:153], v[206:209], v[78:81]
	v_mfma_f32_16x16x32_bf16 v[74:77], v[158:161], v[206:209], v[74:77]
	s_setprio 0
	s_setprio 1
	v_mfma_f32_16x16x32_bf16 v[118:121], v[162:165], v[178:181], v[118:121]
	v_mfma_f32_16x16x32_bf16 v[114:117], v[170:173], v[178:181], v[114:117]
	v_mfma_f32_16x16x32_bf16 v[102:105], v[162:165], v[186:189], v[102:105]
	v_mfma_f32_16x16x32_bf16 v[98:101], v[170:173], v[186:189], v[98:101]
	v_mfma_f32_16x16x32_bf16 v[86:89], v[162:165], v[194:197], v[86:89]
	v_mfma_f32_16x16x32_bf16 v[82:85], v[170:173], v[194:197], v[82:85]
	v_mfma_f32_16x16x32_bf16 v[70:73], v[162:165], v[202:205], v[70:73]
	v_mfma_f32_16x16x32_bf16 v[66:69], v[170:173], v[202:205], v[66:69]
	v_mfma_f32_16x16x32_bf16 v[118:121], v[166:169], v[182:185], v[118:121]
	v_mfma_f32_16x16x32_bf16 v[114:117], v[174:177], v[182:185], v[114:117]
	v_mfma_f32_16x16x32_bf16 v[102:105], v[166:169], v[190:193], v[102:105]
	v_mfma_f32_16x16x32_bf16 v[98:101], v[174:177], v[190:193], v[98:101]
	v_mfma_f32_16x16x32_bf16 v[86:89], v[166:169], v[198:201], v[86:89]
	v_mfma_f32_16x16x32_bf16 v[82:85], v[174:177], v[198:201], v[82:85]
	v_mfma_f32_16x16x32_bf16 v[70:73], v[166:169], v[206:209], v[70:73]
	v_mfma_f32_16x16x32_bf16 v[66:69], v[174:177], v[206:209], v[66:69]
	s_setprio 0
	s_barrier
	s_mov_b32 m0, s17
	v_lshl_add_u64 v[140:141], s[20:21], 0, v[64:65]
	s_add_u32 s52, s20, 0x40000
	ds_read_b128 v[178:181], v145 offset:16384
	ds_read_b128 v[182:185], v145 offset:17408
	ds_read_b128 v[186:189], v145 offset:18432
	ds_read_b128 v[190:193], v145 offset:19456
	ds_read_b128 v[194:197], v145 offset:20480
	ds_read_b128 v[198:201], v145 offset:21504
	ds_read_b128 v[202:205], v145 offset:22528
	ds_read_b128 v[206:209], v145 offset:23552
	global_load_lds_dwordx4 v[140:141], off
	v_lshl_add_u64 v[210:211], s[20:21], 0, v[130:131]
	s_mov_b32 m0, s27
	s_addc_u32 s53, s21, 0
	global_load_lds_dwordx4 v[210:211], off
	v_lshl_add_u64 v[212:213], s[52:53], 0, v[64:65]
	s_mov_b32 m0, s28
	v_lshl_add_u64 v[214:215], s[22:23], 0, v[132:133]
	global_load_lds_dwordx4 v[212:213], off
	v_lshl_add_u64 v[212:213], s[52:53], 0, v[130:131]
	s_mov_b32 m0, s29
	s_nop 0
	global_load_lds_dwordx4 v[212:213], off
	v_lshl_add_u64 v[212:213], s[22:23], 0, v[134:135]
	s_mov_b32 m0, s30
	s_nop 0
	global_load_lds_dwordx4 v[212:213], off
	s_mov_b32 m0, s31
	s_nop 0
	global_load_lds_dwordx4 v[214:215], off
	s_waitcnt vmcnt(8)
	s_waitcnt lgkmcnt(0)
	s_barrier
; #define PG8_STAGE_A(bufoff, kt, h, usenext) do { if constexpr (Sched::GATHER) { unsigned vo_[2] = { (usenext) ? goffN[h][0] : goff[h][0], (usenext) ? goffN[h][1] : goff[h][1] }; PG8_STAGE(bufoff, kt, vo_); } \
;         else { PG8_STAGE(bufoff, (kt) + ((h) ? hstep : 0), voffA); } } while (0)
; #define PG8_LDA(dst, b, h) do { _Pragma("unroll") for (int m = 0; m < 4; ++m) _Pragma("unroll") for (int k = 0; k < 2; ++k) dst[m][k] = *(const LAS bf16x8*)(lds + PG8_SA(b, h) + aoff + m * 2048 + k * 1024); } while (0)
; #define PG8_LDB(dst, b, h) do { _Pragma("unroll") for (int n = 0; n < 2; ++n) _Pragma("unroll") for (int k = 0; k < 2; ++k) dst[n][k] = *(const LAS bf16x8*)(lds + PG8_SB(b, h) + boff + n * 2048 + k * 1024); } while (0)
; #define PG8_MMA(ai, bj, At, Bt) do { __builtin_amdgcn_s_setprio(1); _Pragma("unroll") for (int m = 0; m < 4; ++m) _Pragma("unroll") for (int n = 0; n < 2; ++n) _Pragma("unroll") for (int k = 0; k < 2; ++k) \
;         acc[ai][bj][m][n] = __builtin_amdgcn_mfma_f32_16x16x32_bf16(Bt[n][k], At[m][k], acc[ai][bj][m][n], 0, 0, 0); __builtin_amdgcn_s_setprio(0); } while (0)
; #define PG8_WAIT_V(n) asm volatile("s_waitcnt vmcnt(" #n ")" ::: "memory")
; #define PG8_WAIT_L(n) asm volatile("s_waitcnt lgkmcnt(" #n ")" ::: "memory")
; #define PG8_BAR __builtin_amdgcn_s_barrier()
; #define PG8_SCHED __builtin_amdgcn_sched_barrier(0)
; template <class Epi, class Sched, bool ALIGN_EPI = true, bool SP2 = true>
; __device__ __forceinline__ void gemm_phase(LAS unsigned char* lds, const Gemm g, const Sched& S, const Epi& E, int tid_in) {
;     ...
;             PG8_WAIT_V(8); PG8_WAIT_L(0); PG8_BAR; PG8_MMA(1, 0, At, B0); PG8_MMA(1, 1, At, B1); PG8_BAR; PG8_SCHED;
;             PG8_LDB(B0, 1, 0); PG8_LDB(B1, 1, 1); PG8_SCHED; PG8_LDA(At, 1, 0); PG8_STAGE_A(PG8_SA(0, 1), a2, 1, last);
;             PG8_WAIT_V(8); PG8_WAIT_L(0); PG8_BAR; PG8_MMA(0, 0, At, B0); PG8_MMA(0, 1, At, B1); PG8_BAR; PG8_SCHED;
	s_setprio 1
	s_waitcnt lgkmcnt(0)
	v_mfma_f32_16x16x32_bf16 v[60:63], v[146:149], v[178:181], v[60:63]
	v_mfma_f32_16x16x32_bf16 v[56:59], v[154:157], v[178:181], v[56:59]
	v_mfma_f32_16x16x32_bf16 v[44:47], v[146:149], v[186:189], v[44:47]
	v_mfma_f32_16x16x32_bf16 v[40:43], v[154:157], v[186:189], v[40:43]
	v_mfma_f32_16x16x32_bf16 v[28:31], v[146:149], v[194:197], v[28:31]
	v_mfma_f32_16x16x32_bf16 v[24:27], v[154:157], v[194:197], v[24:27]
	v_mfma_f32_16x16x32_bf16 v[12:15], v[146:149], v[202:205], v[12:15]
	v_mfma_f32_16x16x32_bf16 v[8:11], v[154:157], v[202:205], v[8:11]
	v_mfma_f32_16x16x32_bf16 v[60:63], v[150:153], v[182:185], v[60:63]
	v_mfma_f32_16x16x32_bf16 v[56:59], v[158:161], v[182:185], v[56:59]
	v_mfma_f32_16x16x32_bf16 v[44:47], v[150:153], v[190:193], v[44:47]
	v_mfma_f32_16x16x32_bf16 v[40:43], v[158:161], v[190:193], v[40:43]
	v_mfma_f32_16x16x32_bf16 v[28:31], v[150:153], v[198:201], v[28:31]
	v_mfma_f32_16x16x32_bf16 v[24:27], v[158:161], v[198:201], v[24:27]
	v_mfma_f32_16x16x32_bf16 v[12:15], v[150:153], v[206:209], v[12:15]
	v_mfma_f32_16x16x32_bf16 v[8:11], v[158:161], v[206:209], v[8:11]
	s_setprio 0
	s_setprio 1
	v_mfma_f32_16x16x32_bf16 v[52:55], v[162:165], v[178:181], v[52:55]
	v_mfma_f32_16x16x32_bf16 v[48:51], v[170:173], v[178:181], v[48:51]
	v_mfma_f32_16x16x32_bf16 v[36:39], v[162:165], v[186:189], v[36:39]
	v_mfma_f32_16x16x32_bf16 v[32:35], v[170:173], v[186:189], v[32:35]
	v_mfma_f32_16x16x32_bf16 v[20:23], v[162:165], v[194:197], v[20:23]
	v_mfma_f32_16x16x32_bf16 v[16:19], v[170:173], v[194:197], v[16:19]
	v_mfma_f32_16x16x32_bf16 v[4:7], v[162:165], v[202:205], v[4:7]
	v_mfma_f32_16x16x32_bf16 v[0:3], v[170:173], v[202:205], v[0:3]
	v_mfma_f32_16x16x32_bf16 v[52:55], v[166:169], v[182:185], v[52:55]
	v_mfma_f32_16x16x32_bf16 v[48:51], v[174:177], v[182:185], v[48:51]
	v_mfma_f32_16x16x32_bf16 v[36:39], v[166:169], v[190:193], v[36:39]
	v_mfma_f32_16x16x32_bf16 v[32:35], v[174:177], v[190:193], v[32:35]
	v_mfma_f32_16x16x32_bf16 v[20:23], v[166:169], v[198:201], v[20:23]
	v_mfma_f32_16x16x32_bf16 v[16:19], v[174:177], v[198:201], v[16:19]
	v_mfma_f32_16x16x32_bf16 v[4:7], v[166:169], v[206:209], v[4:7]
	v_mfma_f32_16x16x32_bf16 v[0:3], v[174:177], v[206:209], v[0:3]
	s_setprio 0
	s_barrier
	v_add_u32_e32 v158, s35, v143
	v_add_u32_e32 v174, s36, v143
	ds_read_b128 v[146:149], v158
	ds_read_b128 v[150:153], v158 offset:1024
	ds_read_b128 v[154:157], v158 offset:2048
	ds_read_b128 v[158:161], v158 offset:3072
	ds_read_b128 v[162:165], v174
	ds_read_b128 v[166:169], v174 offset:1024
	ds_read_b128 v[170:173], v174 offset:2048
	ds_read_b128 v[174:177], v174 offset:3072
	s_add_u32 s22, s22, 0x40000
	s_addc_u32 s23, s23, 0
	s_mov_b32 m0, s33
	v_lshl_add_u64 v[216:217], s[22:23], 0, v[134:135]
	ds_read_b128 v[178:181], v145 offset:32768
	ds_read_b128 v[182:185], v145 offset:33792
	ds_read_b128 v[186:189], v145 offset:34816
	ds_read_b128 v[190:193], v145 offset:35840
	ds_read_b128 v[194:197], v145 offset:36864
	ds_read_b128 v[198:201], v145 offset:37888
	ds_read_b128 v[202:205], v145 offset:38912
	ds_read_b128 v[206:209], v145 offset:39936
	global_load_lds_dwordx4 v[216:217], off
	v_lshl_add_u64 v[216:217], s[22:23], 0, v[132:133]
	s_mov_b32 m0, s34
	s_nop 0
	global_load_lds_dwordx4 v[216:217], off
	s_waitcnt vmcnt(8)
	s_waitcnt lgkmcnt(0)
	s_barrier
	s_setprio 1
	s_waitcnt lgkmcnt(0)
	v_mfma_f32_16x16x32_bf16 v[126:129], v[146:149], v[178:181], v[126:129]
	v_mfma_f32_16x16x32_bf16 v[122:125], v[154:157], v[178:181], v[122:125]
	v_mfma_f32_16x16x32_bf16 v[110:113], v[146:149], v[186:189], v[110:113]
	v_mfma_f32_16x16x32_bf16 v[106:109], v[154:157], v[186:189], v[106:109]
	v_mfma_f32_16x16x32_bf16 v[94:97], v[146:149], v[194:197], v[94:97]
	v_mfma_f32_16x16x32_bf16 v[90:93], v[154:157], v[194:197], v[90:93]
	v_mfma_f32_16x16x32_bf16 v[78:81], v[146:149], v[202:205], v[78:81]
	v_mfma_f32_16x16x32_bf16 v[74:77], v[154:157], v[202:205], v[74:77]
	v_mfma_f32_16x16x32_bf16 v[126:129], v[150:153], v[182:185], v[126:129]
	v_mfma_f32_16x16x32_bf16 v[122:125], v[158:161], v[182:185], v[122:125]
	v_mfma_f32_16x16x32_bf16 v[110:113], v[150:153], v[190:193], v[110:113]
	v_mfma_f32_16x16x32_bf16 v[106:109], v[158:161], v[190:193], v[106:109]
	v_mfma_f32_16x16x32_bf16 v[94:97], v[150:153], v[198:201], v[94:97]
	v_mfma_f32_16x16x32_bf16 v[90:93], v[158:161], v[198:201], v[90:93]
	v_mfma_f32_16x16x32_bf16 v[78:81], v[150:153], v[206:209], v[78:81]
	v_mfma_f32_16x16x32_bf16 v[74:77], v[158:161], v[206:209], v[74:77]
	s_setprio 0
	s_setprio 1
	v_mfma_f32_16x16x32_bf16 v[118:121], v[162:165], v[178:181], v[118:121]
	v_mfma_f32_16x16x32_bf16 v[114:117], v[170:173], v[178:181], v[114:117]
	v_mfma_f32_16x16x32_bf16 v[102:105], v[162:165], v[186:189], v[102:105]
	v_mfma_f32_16x16x32_bf16 v[98:101], v[170:173], v[186:189], v[98:101]
	v_mfma_f32_16x16x32_bf16 v[86:89], v[162:165], v[194:197], v[86:89]
	v_mfma_f32_16x16x32_bf16 v[82:85], v[170:173], v[194:197], v[82:85]
	v_mfma_f32_16x16x32_bf16 v[70:73], v[162:165], v[202:205], v[70:73]
	v_mfma_f32_16x16x32_bf16 v[66:69], v[170:173], v[202:205], v[66:69]
	v_mfma_f32_16x16x32_bf16 v[118:121], v[166:169], v[182:185], v[118:121]
	v_mfma_f32_16x16x32_bf16 v[114:117], v[174:177], v[182:185], v[114:117]
	v_mfma_f32_16x16x32_bf16 v[102:105], v[166:169], v[190:193], v[102:105]
	v_mfma_f32_16x16x32_bf16 v[98:101], v[174:177], v[190:193], v[98:101]
	v_mfma_f32_16x16x32_bf16 v[86:89], v[166:169], v[198:201], v[86:89]
	v_mfma_f32_16x16x32_bf16 v[82:85], v[174:177], v[198:201], v[82:85]
	v_mfma_f32_16x16x32_bf16 v[70:73], v[166:169], v[206:209], v[70:73]
	v_mfma_f32_16x16x32_bf16 v[66:69], v[174:177], v[206:209], v[66:69]
	s_setprio 0
	s_barrier
; #define PG8_STAGE_A(bufoff, kt, h, usenext) do { if constexpr (Sched::GATHER) { unsigned vo_[2] = { (usenext) ? goffN[h][0] : goff[h][0], (usenext) ? goffN[h][1] : goff[h][1] }; PG8_STAGE(bufoff, kt, vo_); } \
;         else { PG8_STAGE(bufoff, (kt) + ((h) ? hstep : 0), voffA); } } while (0)
; #define PG8_STAGE(bufoff, gbase, voff) do { _Pragma("unroll") for (int _i = 0; _i < 2; ++_i) \
;         __builtin_amdgcn_global_load_lds((const unsigned*)((const char*)(gbase) + (voff)[_i]), (LAS unsigned*)(lds + (bufoff) + ldsw + _i * 8192), 16, 0, 0); } while (0)
; template <class Epi, class Sched, bool ALIGN_EPI = true, bool SP2 = true>
; __device__ __forceinline__ void gemm_phase(LAS unsigned char* lds, const Gemm g, const Sched& S, const Epi& E, int tid_in) {
;     ...
;             PG8_LDA(At, 1, 1); PG8_STAGE(PG8_SB(1, 0), b3, voffB); PG8_STAGE(PG8_SB(1, 1), b3 + hstepB, voffB); PG8_STAGE_A(PG8_SA(1, 0), a3, 0, last);
;             PG8_WAIT_V(8); PG8_WAIT_L(0); PG8_BAR; PG8_MMA(1, 0, At, B0); PG8_MMA(1, 1, At, B1); PG8_BAR; PG8_SCHED;
;             } else {
;             PG8_LDB(B0, 0, 0); PG8_SCHED; PG8_LDA(At, 0, 0); PG8_STAGE_A(PG8_SA(1, 1), a1, 1, false);
;             PG8_WAIT_L(8); PG8_BAR; PG8_WAIT_L(0); PG8_MMA(0, 0, At, B0); PG8_BAR; PG8_SCHED;
;             PG8_LDB(B1, 0, 1); PG8_STAGE(PG8_SB(0, 0), b2, voffB);
;             PG8_BAR; PG8_WAIT_L(0); PG8_MMA(0, 1, At, B1); PG8_BAR;
;             PG8_LDA(At, 0, 1); PG8_STAGE_A(PG8_SA(0, 0), a2, 0, last);
;             PG8_BAR; PG8_WAIT_L(0); PG8_MMA(1, 0, At, B0); PG8_BAR; PG8_SCHED;
;             PG8_STAGE(PG8_SB(0, 1), b2 + hstepB, voffB);
;             PG8_WAIT_V(6); PG8_BAR; PG8_MMA(1, 1, At, B1); PG8_BAR;
;             PG8_LDB(B0, 1, 0); PG8_SCHED; PG8_LDA(At, 1, 0); PG8_STAGE_A(PG8_SA(0, 1), a2, 1, last);
;             PG8_WAIT_L(8); PG8_BAR; PG8_WAIT_L(0); PG8_MMA(0, 0, At, B0); PG8_BAR; PG8_SCHED;
;             PG8_LDB(B1, 1, 1); PG8_STAGE(PG8_SB(1, 0), b3, voffB);
;             PG8_BAR; PG8_WAIT_L(0); PG8_MMA(0, 1, At, B1); PG8_BAR;
;             PG8_LDA(At, 1, 1); PG8_STAGE_A(PG8_SA(1, 0), a3, 0, last);
;             PG8_BAR; PG8_WAIT_L(0); PG8_MMA(1, 0, At, B0); PG8_BAR; PG8_SCHED;
;             PG8_STAGE(PG8_SB(1, 1), b3 + hstepB, voffB);
;             PG8_WAIT_V(6); PG8_BAR; PG8_MMA(1, 1, At, B1); PG8_BAR;
;             }
;         }
;         if constexpr (ALIGN_EPI) { if (wr == 0) PG8_BAR; }
	s_mov_b32 m0, s38
	v_lshl_add_u64 v[140:141], v[140:141], 0, s[54:55]
	s_add_u32 s20, s20, 0x40080
	ds_read_b128 v[178:181], v145 offset:49152
	ds_read_b128 v[182:185], v145 offset:50176
	ds_read_b128 v[186:189], v145 offset:51200
	ds_read_b128 v[190:193], v145 offset:52224
	ds_read_b128 v[194:197], v145 offset:53248
	ds_read_b128 v[198:201], v145 offset:54272
	ds_read_b128 v[202:205], v145 offset:55296
	ds_read_b128 v[206:209], v145 offset:56320
	global_load_lds_dwordx4 v[140:141], off
	v_lshl_add_u64 v[140:141], v[210:211], 0, s[54:55]
	s_mov_b32 m0, s39
	s_addc_u32 s21, s21, 0
	global_load_lds_dwordx4 v[140:141], off
	v_lshl_add_u64 v[140:141], s[20:21], 0, v[64:65]
	s_mov_b32 m0, s42
	s_nop 0
	global_load_lds_dwordx4 v[140:141], off
	v_lshl_add_u64 v[140:141], s[20:21], 0, v[130:131]
	s_mov_b32 m0, s43
	s_nop 0
	global_load_lds_dwordx4 v[140:141], off
	v_lshl_add_u64 v[140:141], v[212:213], 0, s[54:55]
	s_mov_b32 m0, s40
	s_nop 0
	global_load_lds_dwordx4 v[140:141], off
	v_lshl_add_u64 v[140:141], v[214:215], 0, s[54:55]
	s_mov_b32 m0, s41
	s_nop 0
	global_load_lds_dwordx4 v[140:141], off
	s_waitcnt vmcnt(8)
	s_waitcnt lgkmcnt(0)
	s_barrier
	s_setprio 1
	s_waitcnt lgkmcnt(0)
	v_mfma_f32_16x16x32_bf16 v[60:63], v[146:149], v[178:181], v[60:63]
	v_mfma_f32_16x16x32_bf16 v[56:59], v[154:157], v[178:181], v[56:59]
	v_mfma_f32_16x16x32_bf16 v[44:47], v[146:149], v[186:189], v[44:47]
	v_mfma_f32_16x16x32_bf16 v[40:43], v[154:157], v[186:189], v[40:43]
	v_mfma_f32_16x16x32_bf16 v[28:31], v[146:149], v[194:197], v[28:31]
	v_mfma_f32_16x16x32_bf16 v[24:27], v[154:157], v[194:197], v[24:27]
	v_mfma_f32_16x16x32_bf16 v[12:15], v[146:149], v[202:205], v[12:15]
	v_mfma_f32_16x16x32_bf16 v[8:11], v[154:157], v[202:205], v[8:11]
	v_mfma_f32_16x16x32_bf16 v[60:63], v[150:153], v[182:185], v[60:63]
	v_mfma_f32_16x16x32_bf16 v[56:59], v[158:161], v[182:185], v[56:59]
	v_mfma_f32_16x16x32_bf16 v[44:47], v[150:153], v[190:193], v[44:47]
	v_mfma_f32_16x16x32_bf16 v[40:43], v[158:161], v[190:193], v[40:43]
	v_mfma_f32_16x16x32_bf16 v[28:31], v[150:153], v[198:201], v[28:31]
	v_mfma_f32_16x16x32_bf16 v[24:27], v[158:161], v[198:201], v[24:27]
	v_mfma_f32_16x16x32_bf16 v[12:15], v[150:153], v[206:209], v[12:15]
	v_mfma_f32_16x16x32_bf16 v[8:11], v[158:161], v[206:209], v[8:11]
	s_setprio 0
	s_setprio 1
	v_mfma_f32_16x16x32_bf16 v[52:55], v[162:165], v[178:181], v[52:55]
	v_mfma_f32_16x16x32_bf16 v[48:51], v[170:173], v[178:181], v[48:51]
	v_mfma_f32_16x16x32_bf16 v[36:39], v[162:165], v[186:189], v[36:39]
	v_mfma_f32_16x16x32_bf16 v[32:35], v[170:173], v[186:189], v[32:35]
	v_mfma_f32_16x16x32_bf16 v[20:23], v[162:165], v[194:197], v[20:23]
	v_mfma_f32_16x16x32_bf16 v[16:19], v[170:173], v[194:197], v[16:19]
	v_mfma_f32_16x16x32_bf16 v[4:7], v[162:165], v[202:205], v[4:7]
	v_mfma_f32_16x16x32_bf16 v[0:3], v[170:173], v[202:205], v[0:3]
	v_mfma_f32_16x16x32_bf16 v[52:55], v[166:169], v[182:185], v[52:55]
	v_mfma_f32_16x16x32_bf16 v[48:51], v[174:177], v[182:185], v[48:51]
	v_mfma_f32_16x16x32_bf16 v[36:39], v[166:169], v[190:193], v[36:39]
	v_mfma_f32_16x16x32_bf16 v[32:35], v[174:177], v[190:193], v[32:35]
	v_mfma_f32_16x16x32_bf16 v[20:23], v[166:169], v[198:201], v[20:23]
	v_mfma_f32_16x16x32_bf16 v[16:19], v[174:177], v[198:201], v[16:19]
	v_mfma_f32_16x16x32_bf16 v[4:7], v[166:169], v[206:209], v[4:7]
	v_mfma_f32_16x16x32_bf16 v[0:3], v[174:177], v[206:209], v[0:3]
	s_setprio 0
	s_add_i32 s51, s51, 2
	s_add_u32 s18, s18, 0x100
	s_addc_u32 s19, s19, 0
	s_add_u32 s49, s49, 0x100
	s_addc_u32 s50, s50, 0
	s_cmp_gt_u32 s51, 13
	s_barrier
	s_cbranch_scc0 .LBB0_2333
	s_and_b64 vcc, exec, s[6:7]
	v_readlane_b32 s50, v252, 36
	v_readlane_b32 s51, v252, 37
	s_cbranch_vccz .LBB0_2336
	s_barrier

; #define PG8_STAGE_A(bufoff, kt, h, usenext) do { if constexpr (Sched::GATHER) { unsigned vo_[2] = { (usenext) ? goffN[h][0] : goff[h][0], (usenext) ? goffN[h][1] : goff[h][1] }; PG8_STAGE(bufoff, kt, vo_); } \
;         else { PG8_STAGE(bufoff, (kt) + ((h) ? hstep : 0), voffA); } } while (0)
; #define PG8_STAGE(bufoff, gbase, voff) do { _Pragma("unroll") for (int _i = 0; _i < 2; ++_i) \
;         __builtin_amdgcn_global_load_lds((const unsigned*)((const char*)(gbase) + (voff)[_i]), (LAS unsigned*)(lds + (bufoff) + ldsw + _i * 8192), 16, 0, 0); } while (0)
; #define PG8_LDA(dst, b, h) do { _Pragma("unroll") for (int m = 0; m < 4; ++m) _Pragma("unroll") for (int k = 0; k < 2; ++k) dst[m][k] = *(const LAS bf16x8*)(lds + PG8_SA(b, h) + aoff + m * 2048 + k * 1024); } while (0)
; #define PG8_LDB(dst, b, h) do { _Pragma("unroll") for (int n = 0; n < 2; ++n) _Pragma("unroll") for (int k = 0; k < 2; ++k) dst[n][k] = *(const LAS bf16x8*)(lds + PG8_SB(b, h) + boff + n * 2048 + k * 1024); } while (0)
; #define PG8_MMA(ai, bj, At, Bt) do { __builtin_amdgcn_s_setprio(1); _Pragma("unroll") for (int m = 0; m < 4; ++m) _Pragma("unroll") for (int n = 0; n < 2; ++n) _Pragma("unroll") for (int k = 0; k < 2; ++k) \
;         acc[ai][bj][m][n] = __builtin_amdgcn_mfma_f32_16x16x32_bf16(Bt[n][k], At[m][k], acc[ai][bj][m][n], 0, 0, 0); __builtin_amdgcn_s_setprio(0); } while (0)
; #define PG8_WAIT_V(n) asm volatile("s_waitcnt vmcnt(" #n ")" ::: "memory")
; template <class Epi, class Sched, bool ALIGN_EPI = true, bool SP2 = true>
; __device__ __forceinline__ void gemm_phase(LAS unsigned char* lds, const Gemm g, const Sched& S, const Epi& E, int tid_in) {
;     ...
;             const char* a1 = cA + (size_t)(t + 1) * kstep;
;             const char* a2 = last ? nA : cA + (size_t)(t + 2) * kstep; const char* b2 = last ? nB : cB + (size_t)(t + 2) * kstep;
;             const char* a3 = a2 + kstep; const char* b3 = b2 + kstep;
;             if constexpr (SP2) {
;             PG8_LDB(B0, 0, 0); PG8_LDB(B1, 0, 1); PG8_SCHED; PG8_LDA(At, 0, 0); PG8_STAGE_A(PG8_SA(1, 1), a1, 1, false);
;             PG8_WAIT_V(8); PG8_WAIT_L(0); PG8_BAR; PG8_MMA(0, 0, At, B0); PG8_MMA(0, 1, At, B1); PG8_BAR; PG8_SCHED;
;             PG8_LDA(At, 0, 1); PG8_STAGE(PG8_SB(0, 0), b2, voffB); PG8_STAGE(PG8_SB(0, 1), b2 + hstepB, voffB); PG8_STAGE_A(PG8_SA(0, 0), a2, 0, last);
.LBB0_2487:
	v_add_u32_e32 v142, s31, v175
	v_add_u32_e32 v164, s33, v175
	ds_read_b128 v[130:133], v142
	ds_read_b128 v[134:137], v142 offset:1024
	ds_read_b128 v[138:141], v142 offset:2048
	ds_read_b128 v[142:145], v142 offset:3072
	ds_read_b128 v[146:149], v164
	ds_read_b128 v[150:153], v164 offset:1024
	ds_read_b128 v[154:157], v164 offset:2048
	ds_read_b128 v[164:167], v164 offset:3072
	s_add_u32 s22, s20, 0xfffc0080
	s_addc_u32 s23, s21, -1
	s_cmp_eq_u32 s57, 12
	s_cselect_b32 s25, s13, s23
	s_cselect_b32 s24, s53, s22
	s_cselect_b32 s23, s11, s56
	s_cselect_b32 s22, s54, s55
	v_lshl_add_u64 v[172:173], s[20:21], 0, v[160:161]
	s_add_i32 m0, s38, 0xc000
	ds_read_b128 v[168:171], v177
	ds_read_b128 v[178:181], v177 offset:1024
	ds_read_b128 v[182:185], v177 offset:2048
	ds_read_b128 v[186:189], v177 offset:3072
	ds_read_b128 v[190:193], v177 offset:4096
	ds_read_b128 v[194:197], v177 offset:5120
	ds_read_b128 v[198:201], v177 offset:6144
	ds_read_b128 v[202:205], v177 offset:7168
	global_load_lds_dwordx4 v[172:173], off
	v_lshl_add_u64 v[172:173], s[20:21], 0, v[162:163]
	s_add_i32 m0, s38, 0xe000
	s_nop 0
	global_load_lds_dwordx4 v[172:173], off
	s_waitcnt vmcnt(8)
	s_waitcnt lgkmcnt(0)
	s_barrier
	s_setprio 1
	s_waitcnt lgkmcnt(0)
	v_mfma_f32_16x16x32_bf16 v[126:129], v[130:133], v[168:171], v[126:129]
	v_mfma_f32_16x16x32_bf16 v[122:125], v[138:141], v[168:171], v[122:125]
	v_mfma_f32_16x16x32_bf16 v[118:121], v[130:133], v[182:185], v[118:121]
	v_mfma_f32_16x16x32_bf16 v[106:109], v[138:141], v[182:185], v[106:109]
	v_mfma_f32_16x16x32_bf16 v[102:105], v[130:133], v[190:193], v[102:105]
	v_mfma_f32_16x16x32_bf16 v[90:93], v[138:141], v[190:193], v[90:93]
	v_mfma_f32_16x16x32_bf16 v[86:89], v[130:133], v[198:201], v[86:89]
	v_mfma_f32_16x16x32_bf16 v[74:77], v[138:141], v[198:201], v[74:77]
	v_mfma_f32_16x16x32_bf16 v[126:129], v[134:137], v[178:181], v[126:129]
	v_mfma_f32_16x16x32_bf16 v[122:125], v[142:145], v[178:181], v[122:125]
	v_mfma_f32_16x16x32_bf16 v[118:121], v[134:137], v[186:189], v[118:121]
	v_mfma_f32_16x16x32_bf16 v[106:109], v[142:145], v[186:189], v[106:109]
	v_mfma_f32_16x16x32_bf16 v[102:105], v[134:137], v[194:197], v[102:105]
	v_mfma_f32_16x16x32_bf16 v[90:93], v[142:145], v[194:197], v[90:93]
	v_mfma_f32_16x16x32_bf16 v[86:89], v[134:137], v[202:205], v[86:89]
	v_mfma_f32_16x16x32_bf16 v[74:77], v[142:145], v[202:205], v[74:77]
	s_setprio 0
	s_setprio 1
	v_mfma_f32_16x16x32_bf16 v[114:117], v[146:149], v[168:171], v[114:117]
	v_mfma_f32_16x16x32_bf16 v[110:113], v[154:157], v[168:171], v[110:113]
	v_mfma_f32_16x16x32_bf16 v[98:101], v[146:149], v[182:185], v[98:101]
	v_mfma_f32_16x16x32_bf16 v[94:97], v[154:157], v[182:185], v[94:97]
	v_mfma_f32_16x16x32_bf16 v[82:85], v[146:149], v[190:193], v[82:85]
	v_mfma_f32_16x16x32_bf16 v[78:81], v[154:157], v[190:193], v[78:81]
	v_mfma_f32_16x16x32_bf16 v[70:73], v[146:149], v[198:201], v[70:73]
	v_mfma_f32_16x16x32_bf16 v[66:69], v[154:157], v[198:201], v[66:69]
	v_mfma_f32_16x16x32_bf16 v[114:117], v[150:153], v[178:181], v[114:117]
	v_mfma_f32_16x16x32_bf16 v[110:113], v[164:167], v[178:181], v[110:113]
	v_mfma_f32_16x16x32_bf16 v[98:101], v[150:153], v[186:189], v[98:101]
	v_mfma_f32_16x16x32_bf16 v[94:97], v[164:167], v[186:189], v[94:97]
	v_mfma_f32_16x16x32_bf16 v[82:85], v[150:153], v[194:197], v[82:85]
	v_mfma_f32_16x16x32_bf16 v[78:81], v[164:167], v[194:197], v[78:81]
	v_mfma_f32_16x16x32_bf16 v[70:73], v[150:153], v[202:205], v[70:73]
	v_mfma_f32_16x16x32_bf16 v[66:69], v[164:167], v[202:205], v[66:69]
	s_setprio 0
	s_barrier
	s_mov_b32 m0, s34
	v_lshl_add_u64 v[172:173], s[22:23], 0, v[64:65]
	s_add_u32 s58, s22, 0x40000
	ds_read_b128 v[168:171], v177 offset:16384
	ds_read_b128 v[178:181], v177 offset:17408
	ds_read_b128 v[182:185], v177 offset:18432
	ds_read_b128 v[186:189], v177 offset:19456
	ds_read_b128 v[190:193], v177 offset:20480
	ds_read_b128 v[194:197], v177 offset:21504
	ds_read_b128 v[198:201], v177 offset:22528
	ds_read_b128 v[202:205], v177 offset:23552
	global_load_lds_dwordx4 v[172:173], off
	v_lshl_add_u64 v[206:207], s[22:23], 0, v[158:159]
	s_mov_b32 m0, s35
	s_addc_u32 s59, s23, 0
	global_load_lds_dwordx4 v[206:207], off
	v_lshl_add_u64 v[208:209], s[58:59], 0, v[64:65]
	s_mov_b32 m0, s36
	v_lshl_add_u64 v[210:211], s[24:25], 0, v[158:159]
	global_load_lds_dwordx4 v[208:209], off
	v_lshl_add_u64 v[208:209], s[58:59], 0, v[158:159]
	s_mov_b32 m0, s37
	s_nop 0
	global_load_lds_dwordx4 v[208:209], off
	v_lshl_add_u64 v[208:209], s[24:25], 0, v[64:65]
	s_mov_b32 m0, s38
	s_nop 0
	global_load_lds_dwordx4 v[208:209], off
	s_mov_b32 m0, s39
	s_nop 0
	global_load_lds_dwordx4 v[210:211], off
	s_waitcnt vmcnt(8)
	s_waitcnt lgkmcnt(0)
	s_barrier
; #define PG8_STAGE_A(bufoff, kt, h, usenext) do { if constexpr (Sched::GATHER) { unsigned vo_[2] = { (usenext) ? goffN[h][0] : goff[h][0], (usenext) ? goffN[h][1] : goff[h][1] }; PG8_STAGE(bufoff, kt, vo_); } \
;         else { PG8_STAGE(bufoff, (kt) + ((h) ? hstep : 0), voffA); } } while (0)
; #define PG8_LDA(dst, b, h) do { _Pragma("unroll") for (int m = 0; m < 4; ++m) _Pragma("unroll") for (int k = 0; k < 2; ++k) dst[m][k] = *(const LAS bf16x8*)(lds + PG8_SA(b, h) + aoff + m * 2048 + k * 1024); } while (0)
; #define PG8_LDB(dst, b, h) do { _Pragma("unroll") for (int n = 0; n < 2; ++n) _Pragma("unroll") for (int k = 0; k < 2; ++k) dst[n][k] = *(const LAS bf16x8*)(lds + PG8_SB(b, h) + boff + n * 2048 + k * 1024); } while (0)
; #define PG8_MMA(ai, bj, At, Bt) do { __builtin_amdgcn_s_setprio(1); _Pragma("unroll") for (int m = 0; m < 4; ++m) _Pragma("unroll") for (int n = 0; n < 2; ++n) _Pragma("unroll") for (int k = 0; k < 2; ++k) \
;         acc[ai][bj][m][n] = __builtin_amdgcn_mfma_f32_16x16x32_bf16(Bt[n][k], At[m][k], acc[ai][bj][m][n], 0, 0, 0); __builtin_amdgcn_s_setprio(0); } while (0)
; #define PG8_WAIT_V(n) asm volatile("s_waitcnt vmcnt(" #n ")" ::: "memory")
; #define PG8_WAIT_L(n) asm volatile("s_waitcnt lgkmcnt(" #n ")" ::: "memory")
; #define PG8_BAR __builtin_amdgcn_s_barrier()
; #define PG8_SCHED __builtin_amdgcn_sched_barrier(0)
; template <class Epi, class Sched, bool ALIGN_EPI = true, bool SP2 = true>
; __device__ __forceinline__ void gemm_phase(LAS unsigned char* lds, const Gemm g, const Sched& S, const Epi& E, int tid_in) {
;     ...
;             PG8_WAIT_V(8); PG8_WAIT_L(0); PG8_BAR; PG8_MMA(1, 0, At, B0); PG8_MMA(1, 1, At, B1); PG8_BAR; PG8_SCHED;
;             PG8_LDB(B0, 1, 0); PG8_LDB(B1, 1, 1); PG8_SCHED; PG8_LDA(At, 1, 0); PG8_STAGE_A(PG8_SA(0, 1), a2, 1, last);
;             PG8_WAIT_V(8); PG8_WAIT_L(0); PG8_BAR; PG8_MMA(0, 0, At, B0); PG8_MMA(0, 1, At, B1); PG8_BAR; PG8_SCHED;
	s_setprio 1
	s_waitcnt lgkmcnt(0)
	v_mfma_f32_16x16x32_bf16 v[60:63], v[130:133], v[168:171], v[60:63]
	v_mfma_f32_16x16x32_bf16 v[56:59], v[138:141], v[168:171], v[56:59]
	v_mfma_f32_16x16x32_bf16 v[52:55], v[130:133], v[182:185], v[52:55]
	v_mfma_f32_16x16x32_bf16 v[40:43], v[138:141], v[182:185], v[40:43]
	v_mfma_f32_16x16x32_bf16 v[36:39], v[130:133], v[190:193], v[36:39]
	v_mfma_f32_16x16x32_bf16 v[24:27], v[138:141], v[190:193], v[24:27]
	v_mfma_f32_16x16x32_bf16 v[20:23], v[130:133], v[198:201], v[20:23]
	v_mfma_f32_16x16x32_bf16 v[8:11], v[138:141], v[198:201], v[8:11]
	v_mfma_f32_16x16x32_bf16 v[60:63], v[134:137], v[178:181], v[60:63]
	v_mfma_f32_16x16x32_bf16 v[56:59], v[142:145], v[178:181], v[56:59]
	v_mfma_f32_16x16x32_bf16 v[52:55], v[134:137], v[186:189], v[52:55]
	v_mfma_f32_16x16x32_bf16 v[40:43], v[142:145], v[186:189], v[40:43]
	v_mfma_f32_16x16x32_bf16 v[36:39], v[134:137], v[194:197], v[36:39]
	v_mfma_f32_16x16x32_bf16 v[24:27], v[142:145], v[194:197], v[24:27]
	v_mfma_f32_16x16x32_bf16 v[20:23], v[134:137], v[202:205], v[20:23]
	v_mfma_f32_16x16x32_bf16 v[8:11], v[142:145], v[202:205], v[8:11]
	s_setprio 0
	s_setprio 1
	v_mfma_f32_16x16x32_bf16 v[48:51], v[146:149], v[168:171], v[48:51]
	v_mfma_f32_16x16x32_bf16 v[44:47], v[154:157], v[168:171], v[44:47]
	v_mfma_f32_16x16x32_bf16 v[32:35], v[146:149], v[182:185], v[32:35]
	v_mfma_f32_16x16x32_bf16 v[28:31], v[154:157], v[182:185], v[28:31]
	v_mfma_f32_16x16x32_bf16 v[16:19], v[146:149], v[190:193], v[16:19]
	v_mfma_f32_16x16x32_bf16 v[12:15], v[154:157], v[190:193], v[12:15]
	v_mfma_f32_16x16x32_bf16 v[4:7], v[146:149], v[198:201], v[4:7]
	v_mfma_f32_16x16x32_bf16 v[0:3], v[154:157], v[198:201], v[0:3]
	v_mfma_f32_16x16x32_bf16 v[48:51], v[150:153], v[178:181], v[48:51]
	v_mfma_f32_16x16x32_bf16 v[44:47], v[164:167], v[178:181], v[44:47]
	v_mfma_f32_16x16x32_bf16 v[32:35], v[150:153], v[186:189], v[32:35]
	v_mfma_f32_16x16x32_bf16 v[28:31], v[164:167], v[186:189], v[28:31]
	v_mfma_f32_16x16x32_bf16 v[16:19], v[150:153], v[194:197], v[16:19]
	v_mfma_f32_16x16x32_bf16 v[12:15], v[164:167], v[194:197], v[12:15]
	v_mfma_f32_16x16x32_bf16 v[4:7], v[150:153], v[202:205], v[4:7]
	v_mfma_f32_16x16x32_bf16 v[0:3], v[164:167], v[202:205], v[0:3]
	s_setprio 0
	s_barrier
	v_add_u32_e32 v142, s42, v175
	v_add_u32_e32 v164, s43, v175
	ds_read_b128 v[130:133], v142
	ds_read_b128 v[134:137], v142 offset:1024
	ds_read_b128 v[138:141], v142 offset:2048
	ds_read_b128 v[142:145], v142 offset:3072
	ds_read_b128 v[146:149], v164
	ds_read_b128 v[150:153], v164 offset:1024
	ds_read_b128 v[154:157], v164 offset:2048
	ds_read_b128 v[164:167], v164 offset:3072
	s_add_u32 s24, s24, 0x40000
	s_addc_u32 s25, s25, 0
	s_mov_b32 m0, s40
	v_lshl_add_u64 v[212:213], s[24:25], 0, v[64:65]
	ds_read_b128 v[168:171], v177 offset:32768
	ds_read_b128 v[178:181], v177 offset:33792
	ds_read_b128 v[182:185], v177 offset:34816
	ds_read_b128 v[186:189], v177 offset:35840
	ds_read_b128 v[190:193], v177 offset:36864
	ds_read_b128 v[194:197], v177 offset:37888
	ds_read_b128 v[198:201], v177 offset:38912
	ds_read_b128 v[202:205], v177 offset:39936
	global_load_lds_dwordx4 v[212:213], off
	v_lshl_add_u64 v[212:213], s[24:25], 0, v[158:159]
	s_mov_b32 m0, s41
	s_nop 0
	global_load_lds_dwordx4 v[212:213], off
	s_waitcnt vmcnt(8)
	s_waitcnt lgkmcnt(0)
	s_barrier
	s_setprio 1
	s_waitcnt lgkmcnt(0)
	v_mfma_f32_16x16x32_bf16 v[126:129], v[130:133], v[168:171], v[126:129]
	v_mfma_f32_16x16x32_bf16 v[122:125], v[138:141], v[168:171], v[122:125]
	v_mfma_f32_16x16x32_bf16 v[118:121], v[130:133], v[182:185], v[118:121]
	v_mfma_f32_16x16x32_bf16 v[106:109], v[138:141], v[182:185], v[106:109]
	v_mfma_f32_16x16x32_bf16 v[102:105], v[130:133], v[190:193], v[102:105]
	v_mfma_f32_16x16x32_bf16 v[90:93], v[138:141], v[190:193], v[90:93]
	v_mfma_f32_16x16x32_bf16 v[86:89], v[130:133], v[198:201], v[86:89]
	v_mfma_f32_16x16x32_bf16 v[74:77], v[138:141], v[198:201], v[74:77]
	v_mfma_f32_16x16x32_bf16 v[126:129], v[134:137], v[178:181], v[126:129]
	v_mfma_f32_16x16x32_bf16 v[122:125], v[142:145], v[178:181], v[122:125]
	v_mfma_f32_16x16x32_bf16 v[118:121], v[134:137], v[186:189], v[118:121]
	v_mfma_f32_16x16x32_bf16 v[106:109], v[142:145], v[186:189], v[106:109]
	v_mfma_f32_16x16x32_bf16 v[102:105], v[134:137], v[194:197], v[102:105]
	v_mfma_f32_16x16x32_bf16 v[90:93], v[142:145], v[194:197], v[90:93]
	v_mfma_f32_16x16x32_bf16 v[86:89], v[134:137], v[202:205], v[86:89]
	v_mfma_f32_16x16x32_bf16 v[74:77], v[142:145], v[202:205], v[74:77]
	s_setprio 0
	s_setprio 1
	v_mfma_f32_16x16x32_bf16 v[114:117], v[146:149], v[168:171], v[114:117]
	v_mfma_f32_16x16x32_bf16 v[110:113], v[154:157], v[168:171], v[110:113]
	v_mfma_f32_16x16x32_bf16 v[98:101], v[146:149], v[182:185], v[98:101]
	v_mfma_f32_16x16x32_bf16 v[94:97], v[154:157], v[182:185], v[94:97]
	v_mfma_f32_16x16x32_bf16 v[82:85], v[146:149], v[190:193], v[82:85]
	v_mfma_f32_16x16x32_bf16 v[78:81], v[154:157], v[190:193], v[78:81]
	v_mfma_f32_16x16x32_bf16 v[70:73], v[146:149], v[198:201], v[70:73]
	v_mfma_f32_16x16x32_bf16 v[66:69], v[154:157], v[198:201], v[66:69]
	v_mfma_f32_16x16x32_bf16 v[114:117], v[150:153], v[178:181], v[114:117]
	v_mfma_f32_16x16x32_bf16 v[110:113], v[164:167], v[178:181], v[110:113]
	v_mfma_f32_16x16x32_bf16 v[98:101], v[150:153], v[186:189], v[98:101]
	v_mfma_f32_16x16x32_bf16 v[94:97], v[164:167], v[186:189], v[94:97]
	v_mfma_f32_16x16x32_bf16 v[82:85], v[150:153], v[194:197], v[82:85]
	v_mfma_f32_16x16x32_bf16 v[78:81], v[164:167], v[194:197], v[78:81]
	v_mfma_f32_16x16x32_bf16 v[70:73], v[150:153], v[202:205], v[70:73]
	v_mfma_f32_16x16x32_bf16 v[66:69], v[164:167], v[202:205], v[66:69]
	s_setprio 0
	s_barrier
; #define PG8_STAGE_A(bufoff, kt, h, usenext) do { if constexpr (Sched::GATHER) { unsigned vo_[2] = { (usenext) ? goffN[h][0] : goff[h][0], (usenext) ? goffN[h][1] : goff[h][1] }; PG8_STAGE(bufoff, kt, vo_); } \
;         else { PG8_STAGE(bufoff, (kt) + ((h) ? hstep : 0), voffA); } } while (0)
; #define PG8_STAGE(bufoff, gbase, voff) do { _Pragma("unroll") for (int _i = 0; _i < 2; ++_i) \
;         __builtin_amdgcn_global_load_lds((const unsigned*)((const char*)(gbase) + (voff)[_i]), (LAS unsigned*)(lds + (bufoff) + ldsw + _i * 8192), 16, 0, 0); } while (0)
; template <class Epi, class Sched, bool ALIGN_EPI = true, bool SP2 = true>
; __device__ __forceinline__ void gemm_phase(LAS unsigned char* lds, const Gemm g, const Sched& S, const Epi& E, int tid_in) {
;     ...
;             PG8_LDA(At, 1, 1); PG8_STAGE(PG8_SB(1, 0), b3, voffB); PG8_STAGE(PG8_SB(1, 1), b3 + hstepB, voffB); PG8_STAGE_A(PG8_SA(1, 0), a3, 0, last);
;             PG8_WAIT_V(8); PG8_WAIT_L(0); PG8_BAR; PG8_MMA(1, 0, At, B0); PG8_MMA(1, 1, At, B1); PG8_BAR; PG8_SCHED;
;             } else {
;             PG8_LDB(B0, 0, 0); PG8_SCHED; PG8_LDA(At, 0, 0); PG8_STAGE_A(PG8_SA(1, 1), a1, 1, false);
;             PG8_WAIT_L(8); PG8_BAR; PG8_WAIT_L(0); PG8_MMA(0, 0, At, B0); PG8_BAR; PG8_SCHED;
;             PG8_LDB(B1, 0, 1); PG8_STAGE(PG8_SB(0, 0), b2, voffB);
;             PG8_BAR; PG8_WAIT_L(0); PG8_MMA(0, 1, At, B1); PG8_BAR;
;             PG8_LDA(At, 0, 1); PG8_STAGE_A(PG8_SA(0, 0), a2, 0, last);
;             PG8_BAR; PG8_WAIT_L(0); PG8_MMA(1, 0, At, B0); PG8_BAR; PG8_SCHED;
;             PG8_STAGE(PG8_SB(0, 1), b2 + hstepB, voffB);
;             PG8_WAIT_V(6); PG8_BAR; PG8_MMA(1, 1, At, B1); PG8_BAR;
;             PG8_LDB(B0, 1, 0); PG8_SCHED; PG8_LDA(At, 1, 0); PG8_STAGE_A(PG8_SA(0, 1), a2, 1, last);
;             PG8_WAIT_L(8); PG8_BAR; PG8_WAIT_L(0); PG8_MMA(0, 0, At, B0); PG8_BAR; PG8_SCHED;
;             PG8_LDB(B1, 1, 1); PG8_STAGE(PG8_SB(1, 0), b3, voffB);
;             PG8_BAR; PG8_WAIT_L(0); PG8_MMA(0, 1, At, B1); PG8_BAR;
;             PG8_LDA(At, 1, 1); PG8_STAGE_A(PG8_SA(1, 0), a3, 0, last);
;             PG8_BAR; PG8_WAIT_L(0); PG8_MMA(1, 0, At, B0); PG8_BAR; PG8_SCHED;
;             PG8_STAGE(PG8_SB(1, 1), b3 + hstepB, voffB);
;             PG8_WAIT_V(6); PG8_BAR; PG8_MMA(1, 1, At, B1); PG8_BAR;
;             }
;         }
;         if constexpr (ALIGN_EPI) { if (wr == 0) PG8_BAR; }
	s_mov_b32 m0, s46
	v_lshl_add_u64 v[172:173], v[172:173], 0, s[60:61]
	s_add_u32 s22, s22, 0x40080
	ds_read_b128 v[168:171], v177 offset:49152
	ds_read_b128 v[178:181], v177 offset:50176
	ds_read_b128 v[182:185], v177 offset:51200
	ds_read_b128 v[186:189], v177 offset:52224
	ds_read_b128 v[190:193], v177 offset:53248
	ds_read_b128 v[194:197], v177 offset:54272
	ds_read_b128 v[198:201], v177 offset:55296
	ds_read_b128 v[202:205], v177 offset:56320
	global_load_lds_dwordx4 v[172:173], off
	v_lshl_add_u64 v[172:173], v[206:207], 0, s[60:61]
	s_mov_b32 m0, s47
	s_addc_u32 s23, s23, 0
	global_load_lds_dwordx4 v[172:173], off
	v_lshl_add_u64 v[172:173], s[22:23], 0, v[64:65]
	s_mov_b32 m0, s50
	s_nop 0
	global_load_lds_dwordx4 v[172:173], off
	v_lshl_add_u64 v[172:173], s[22:23], 0, v[158:159]
	s_mov_b32 m0, s51
	s_nop 0
	global_load_lds_dwordx4 v[172:173], off
	v_lshl_add_u64 v[172:173], v[208:209], 0, s[60:61]
	s_mov_b32 m0, s48
	s_nop 0
	global_load_lds_dwordx4 v[172:173], off
	v_lshl_add_u64 v[172:173], v[210:211], 0, s[60:61]
	s_mov_b32 m0, s49
	s_nop 0
	global_load_lds_dwordx4 v[172:173], off
	s_waitcnt vmcnt(8)
	s_waitcnt lgkmcnt(0)
	s_barrier
	s_setprio 1
	s_waitcnt lgkmcnt(0)
	v_mfma_f32_16x16x32_bf16 v[60:63], v[130:133], v[168:171], v[60:63]
	v_mfma_f32_16x16x32_bf16 v[56:59], v[138:141], v[168:171], v[56:59]
	v_mfma_f32_16x16x32_bf16 v[52:55], v[130:133], v[182:185], v[52:55]
	v_mfma_f32_16x16x32_bf16 v[40:43], v[138:141], v[182:185], v[40:43]
	v_mfma_f32_16x16x32_bf16 v[36:39], v[130:133], v[190:193], v[36:39]
	v_mfma_f32_16x16x32_bf16 v[24:27], v[138:141], v[190:193], v[24:27]
	v_mfma_f32_16x16x32_bf16 v[20:23], v[130:133], v[198:201], v[20:23]
	v_mfma_f32_16x16x32_bf16 v[8:11], v[138:141], v[198:201], v[8:11]
	v_mfma_f32_16x16x32_bf16 v[60:63], v[134:137], v[178:181], v[60:63]
	v_mfma_f32_16x16x32_bf16 v[56:59], v[142:145], v[178:181], v[56:59]
	v_mfma_f32_16x16x32_bf16 v[52:55], v[134:137], v[186:189], v[52:55]
	v_mfma_f32_16x16x32_bf16 v[40:43], v[142:145], v[186:189], v[40:43]
	v_mfma_f32_16x16x32_bf16 v[36:39], v[134:137], v[194:197], v[36:39]
	v_mfma_f32_16x16x32_bf16 v[24:27], v[142:145], v[194:197], v[24:27]
	v_mfma_f32_16x16x32_bf16 v[20:23], v[134:137], v[202:205], v[20:23]
	v_mfma_f32_16x16x32_bf16 v[8:11], v[142:145], v[202:205], v[8:11]
	s_setprio 0
	s_setprio 1
	v_mfma_f32_16x16x32_bf16 v[48:51], v[146:149], v[168:171], v[48:51]
	v_mfma_f32_16x16x32_bf16 v[44:47], v[154:157], v[168:171], v[44:47]
	v_mfma_f32_16x16x32_bf16 v[32:35], v[146:149], v[182:185], v[32:35]
	v_mfma_f32_16x16x32_bf16 v[28:31], v[154:157], v[182:185], v[28:31]
	v_mfma_f32_16x16x32_bf16 v[16:19], v[146:149], v[190:193], v[16:19]
	v_mfma_f32_16x16x32_bf16 v[12:15], v[154:157], v[190:193], v[12:15]
	v_mfma_f32_16x16x32_bf16 v[4:7], v[146:149], v[198:201], v[4:7]
	v_mfma_f32_16x16x32_bf16 v[0:3], v[154:157], v[198:201], v[0:3]
	v_mfma_f32_16x16x32_bf16 v[48:51], v[150:153], v[178:181], v[48:51]
	v_mfma_f32_16x16x32_bf16 v[44:47], v[164:167], v[178:181], v[44:47]
	v_mfma_f32_16x16x32_bf16 v[32:35], v[150:153], v[186:189], v[32:35]
	v_mfma_f32_16x16x32_bf16 v[28:31], v[164:167], v[186:189], v[28:31]
	v_mfma_f32_16x16x32_bf16 v[16:19], v[150:153], v[194:197], v[16:19]
	v_mfma_f32_16x16x32_bf16 v[12:15], v[164:167], v[194:197], v[12:15]
	v_mfma_f32_16x16x32_bf16 v[4:7], v[150:153], v[202:205], v[4:7]
	v_mfma_f32_16x16x32_bf16 v[0:3], v[164:167], v[202:205], v[0:3]
	s_setprio 0
	s_add_i32 s57, s57, 2
	s_add_u32 s20, s20, 0x100
	s_addc_u32 s21, s21, 0
	s_add_u32 s55, s55, 0x100
	s_addc_u32 s56, s56, 0
	s_cmp_gt_u32 s57, 13
	s_barrier
	s_cbranch_scc0 .LBB0_2487
	s_and_b64 vcc, exec, s[8:9]
	s_cbranch_vccz .LBB0_2490
	s_barrier

; #define PG8_STAGE_A(bufoff, kt, h, usenext) do { if constexpr (Sched::GATHER) { unsigned vo_[2] = { (usenext) ? goffN[h][0] : goff[h][0], (usenext) ? goffN[h][1] : goff[h][1] }; PG8_STAGE(bufoff, kt, vo_); } \
;         else { PG8_STAGE(bufoff, (kt) + ((h) ? hstep : 0), voffA); } } while (0)
; #define PG8_STAGE(bufoff, gbase, voff) do { _Pragma("unroll") for (int _i = 0; _i < 2; ++_i) \
;         __builtin_amdgcn_global_load_lds((const unsigned*)((const char*)(gbase) + (voff)[_i]), (LAS unsigned*)(lds + (bufoff) + ldsw + _i * 8192), 16, 0, 0); } while (0)
; #define PG8_LDA(dst, b, h) do { _Pragma("unroll") for (int m = 0; m < 4; ++m) _Pragma("unroll") for (int k = 0; k < 2; ++k) dst[m][k] = *(const LAS bf16x8*)(lds + PG8_SA(b, h) + aoff + m * 2048 + k * 1024); } while (0)
; #define PG8_LDB(dst, b, h) do { _Pragma("unroll") for (int n = 0; n < 2; ++n) _Pragma("unroll") for (int k = 0; k < 2; ++k) dst[n][k] = *(const LAS bf16x8*)(lds + PG8_SB(b, h) + boff + n * 2048 + k * 1024); } while (0)
; #define PG8_MMA(ai, bj, At, Bt) do { __builtin_amdgcn_s_setprio(1); _Pragma("unroll") for (int m = 0; m < 4; ++m) _Pragma("unroll") for (int n = 0; n < 2; ++n) _Pragma("unroll") for (int k = 0; k < 2; ++k) \
;         acc[ai][bj][m][n] = __builtin_amdgcn_mfma_f32_16x16x32_bf16(Bt[n][k], At[m][k], acc[ai][bj][m][n], 0, 0, 0); __builtin_amdgcn_s_setprio(0); } while (0)
; #define PG8_WAIT_V(n) asm volatile("s_waitcnt vmcnt(" #n ")" ::: "memory")
; template <class Epi, class Sched, bool ALIGN_EPI = true, bool SP2 = true>
; __device__ __forceinline__ void gemm_phase(LAS unsigned char* lds, const Gemm g, const Sched& S, const Epi& E, int tid_in) {
;     ...
;             const char* a1 = cA + (size_t)(t + 1) * kstep;
;             const char* a2 = last ? nA : cA + (size_t)(t + 2) * kstep; const char* b2 = last ? nB : cB + (size_t)(t + 2) * kstep;
;             const char* a3 = a2 + kstep; const char* b3 = b2 + kstep;
;             if constexpr (SP2) {
;             PG8_LDB(B0, 0, 0); PG8_LDB(B1, 0, 1); PG8_SCHED; PG8_LDA(At, 0, 0); PG8_STAGE_A(PG8_SA(1, 1), a1, 1, false);
;             PG8_WAIT_V(8); PG8_WAIT_L(0); PG8_BAR; PG8_MMA(0, 0, At, B0); PG8_MMA(0, 1, At, B1); PG8_BAR; PG8_SCHED;
;             PG8_LDA(At, 0, 1); PG8_STAGE(PG8_SB(0, 0), b2, voffB); PG8_STAGE(PG8_SB(0, 1), b2 + hstepB, voffB); PG8_STAGE_A(PG8_SA(0, 0), a2, 0, last);
.LBB0_2933:
	s_add_u32 s30, s94, s2
	v_add_u32_e32 v64, s47, v161
	s_addc_u32 s31, s95, s3
	ds_read_b128 v[152:155], v64
	ds_read_b128 v[168:171], v64 offset:1024
	ds_read_b128 v[172:175], v64 offset:2048
	ds_read_b128 v[176:179], v64 offset:3072
	v_add_u32_e32 v64, s48, v161
	s_add_u32 s34, s30, 0x8200100
	ds_read_b128 v[180:183], v64
	ds_read_b128 v[184:187], v64 offset:1024
	ds_read_b128 v[188:191], v64 offset:2048
	ds_read_b128 v[192:195], v64 offset:3072
	s_addc_u32 s35, s31, 0
	s_add_u32 s70, s67, s2
	s_addc_u32 s71, s68, s3
	s_cmpk_eq_i32 s2, 0x700
	s_cselect_b64 vcc, -1, 0
	s_and_b64 s[30:31], vcc, exec
	s_cselect_b32 s35, s9, s35
	s_cselect_b32 s34, s8, s34
	s_cselect_b32 s31, s23, s71
	s_cselect_b32 s30, s25, s70
	v_lshl_add_u64 v[148:149], v[144:145], 0, s[2:3]
	s_add_i32 m0, s52, 0xc000
	ds_read_b128 v[196:199], v162
	ds_read_b128 v[200:203], v162 offset:1024
	ds_read_b128 v[204:207], v162 offset:2048
	ds_read_b128 v[208:211], v162 offset:3072
	ds_read_b128 v[212:215], v162 offset:4096
	ds_read_b128 v[216:219], v162 offset:5120
	ds_read_b128 v[220:223], v162 offset:6144
	ds_read_b128 v[226:229], v162 offset:7168
	global_load_lds_dwordx4 v[148:149], off
	v_lshl_add_u64 v[148:149], v[142:143], 0, s[2:3]
	s_add_i32 m0, s52, 0xe000
	s_nop 0
	global_load_lds_dwordx4 v[148:149], off
	s_waitcnt vmcnt(8)
	s_waitcnt lgkmcnt(0)
	s_barrier
	s_setprio 1
	s_waitcnt lgkmcnt(0)
	v_mfma_f32_16x16x32_bf16 v[126:129], v[152:155], v[196:199], v[126:129]
	v_mfma_f32_16x16x32_bf16 v[122:125], v[172:175], v[196:199], v[122:125]
	v_mfma_f32_16x16x32_bf16 v[110:113], v[152:155], v[204:207], v[110:113]
	v_mfma_f32_16x16x32_bf16 v[106:109], v[172:175], v[204:207], v[106:109]
	v_mfma_f32_16x16x32_bf16 v[94:97], v[152:155], v[212:215], v[94:97]
	v_mfma_f32_16x16x32_bf16 v[90:93], v[172:175], v[212:215], v[90:93]
	v_mfma_f32_16x16x32_bf16 v[78:81], v[152:155], v[220:223], v[78:81]
	v_mfma_f32_16x16x32_bf16 v[74:77], v[172:175], v[220:223], v[74:77]
	v_mfma_f32_16x16x32_bf16 v[126:129], v[168:171], v[200:203], v[126:129]
	v_mfma_f32_16x16x32_bf16 v[122:125], v[176:179], v[200:203], v[122:125]
	v_mfma_f32_16x16x32_bf16 v[110:113], v[168:171], v[208:211], v[110:113]
	v_mfma_f32_16x16x32_bf16 v[106:109], v[176:179], v[208:211], v[106:109]
	v_mfma_f32_16x16x32_bf16 v[94:97], v[168:171], v[216:219], v[94:97]
	v_mfma_f32_16x16x32_bf16 v[90:93], v[176:179], v[216:219], v[90:93]
	v_mfma_f32_16x16x32_bf16 v[78:81], v[168:171], v[226:229], v[78:81]
	v_mfma_f32_16x16x32_bf16 v[74:77], v[176:179], v[226:229], v[74:77]
	s_setprio 0
	s_setprio 1
	v_mfma_f32_16x16x32_bf16 v[118:121], v[180:183], v[196:199], v[118:121]
	v_mfma_f32_16x16x32_bf16 v[114:117], v[188:191], v[196:199], v[114:117]
	v_mfma_f32_16x16x32_bf16 v[102:105], v[180:183], v[204:207], v[102:105]
	v_mfma_f32_16x16x32_bf16 v[98:101], v[188:191], v[204:207], v[98:101]
	v_mfma_f32_16x16x32_bf16 v[86:89], v[180:183], v[212:215], v[86:89]
	v_mfma_f32_16x16x32_bf16 v[82:85], v[188:191], v[212:215], v[82:85]
	v_mfma_f32_16x16x32_bf16 v[70:73], v[180:183], v[220:223], v[70:73]
	v_mfma_f32_16x16x32_bf16 v[66:69], v[188:191], v[220:223], v[66:69]
	v_mfma_f32_16x16x32_bf16 v[118:121], v[184:187], v[200:203], v[118:121]
	v_mfma_f32_16x16x32_bf16 v[114:117], v[192:195], v[200:203], v[114:117]
	v_mfma_f32_16x16x32_bf16 v[102:105], v[184:187], v[208:211], v[102:105]
	v_mfma_f32_16x16x32_bf16 v[98:101], v[192:195], v[208:211], v[98:101]
	v_mfma_f32_16x16x32_bf16 v[86:89], v[184:187], v[216:219], v[86:89]
	v_mfma_f32_16x16x32_bf16 v[82:85], v[192:195], v[216:219], v[82:85]
	v_mfma_f32_16x16x32_bf16 v[70:73], v[184:187], v[226:229], v[70:73]
	v_mfma_f32_16x16x32_bf16 v[66:69], v[192:195], v[226:229], v[66:69]
	s_setprio 0
	s_barrier
	s_mov_b32 m0, s29
	v_lshl_add_u64 v[148:149], s[30:31], 0, v[130:131]
	s_add_u32 s70, s30, 0x40000
	ds_read_b128 v[196:199], v162 offset:16384
	ds_read_b128 v[200:203], v162 offset:17408
	ds_read_b128 v[204:207], v162 offset:18432
	ds_read_b128 v[208:211], v162 offset:19456
	ds_read_b128 v[212:215], v162 offset:20480
	ds_read_b128 v[216:219], v162 offset:21504
	ds_read_b128 v[220:223], v162 offset:22528
	ds_read_b128 v[226:229], v162 offset:23552
	global_load_lds_dwordx4 v[148:149], off
	v_lshl_add_u64 v[234:235], s[30:31], 0, v[132:133]
	s_mov_b32 m0, s49
	s_addc_u32 s71, s31, 0
	global_load_lds_dwordx4 v[234:235], off
	v_lshl_add_u64 v[236:237], s[70:71], 0, v[130:131]
	s_mov_b32 m0, s50
	v_cndmask_b32_e32 v64, v140, v163, vcc
	global_load_lds_dwordx4 v[236:237], off
	v_lshl_add_u64 v[236:237], s[70:71], 0, v[132:133]
	s_mov_b32 m0, s51
	v_lshl_add_u64 v[238:239], s[34:35], 0, v[64:65]
	global_load_lds_dwordx4 v[236:237], off
	s_mov_b32 m0, s52
	v_cndmask_b32_e32 v236, v138, v164, vcc
	global_load_lds_dwordx4 v64, s[34:35]
	s_mov_b32 m0, s53
	v_mov_b32_e32 v237, v65
	global_load_lds_dwordx4 v236, s[34:35]
	s_waitcnt vmcnt(8)
	s_waitcnt lgkmcnt(0)
	v_lshl_add_u64 v[236:237], s[34:35], 0, v[236:237]
	s_barrier
; #define PG8_STAGE_A(bufoff, kt, h, usenext) do { if constexpr (Sched::GATHER) { unsigned vo_[2] = { (usenext) ? goffN[h][0] : goff[h][0], (usenext) ? goffN[h][1] : goff[h][1] }; PG8_STAGE(bufoff, kt, vo_); } \
;         else { PG8_STAGE(bufoff, (kt) + ((h) ? hstep : 0), voffA); } } while (0)
; #define PG8_LDA(dst, b, h) do { _Pragma("unroll") for (int m = 0; m < 4; ++m) _Pragma("unroll") for (int k = 0; k < 2; ++k) dst[m][k] = *(const LAS bf16x8*)(lds + PG8_SA(b, h) + aoff + m * 2048 + k * 1024); } while (0)
; #define PG8_LDB(dst, b, h) do { _Pragma("unroll") for (int n = 0; n < 2; ++n) _Pragma("unroll") for (int k = 0; k < 2; ++k) dst[n][k] = *(const LAS bf16x8*)(lds + PG8_SB(b, h) + boff + n * 2048 + k * 1024); } while (0)
; #define PG8_MMA(ai, bj, At, Bt) do { __builtin_amdgcn_s_setprio(1); _Pragma("unroll") for (int m = 0; m < 4; ++m) _Pragma("unroll") for (int n = 0; n < 2; ++n) _Pragma("unroll") for (int k = 0; k < 2; ++k) \
;         acc[ai][bj][m][n] = __builtin_amdgcn_mfma_f32_16x16x32_bf16(Bt[n][k], At[m][k], acc[ai][bj][m][n], 0, 0, 0); __builtin_amdgcn_s_setprio(0); } while (0)
; #define PG8_WAIT_V(n) asm volatile("s_waitcnt vmcnt(" #n ")" ::: "memory")
; #define PG8_WAIT_L(n) asm volatile("s_waitcnt lgkmcnt(" #n ")" ::: "memory")
; #define PG8_BAR __builtin_amdgcn_s_barrier()
; #define PG8_SCHED __builtin_amdgcn_sched_barrier(0)
; template <class Epi, class Sched, bool ALIGN_EPI = true, bool SP2 = true>
; __device__ __forceinline__ void gemm_phase(LAS unsigned char* lds, const Gemm g, const Sched& S, const Epi& E, int tid_in) {
;     ...
;             PG8_WAIT_V(8); PG8_WAIT_L(0); PG8_BAR; PG8_MMA(1, 0, At, B0); PG8_MMA(1, 1, At, B1); PG8_BAR; PG8_SCHED;
;             PG8_LDB(B0, 1, 0); PG8_LDB(B1, 1, 1); PG8_SCHED; PG8_LDA(At, 1, 0); PG8_STAGE_A(PG8_SA(0, 1), a2, 1, last);
;             PG8_WAIT_V(8); PG8_WAIT_L(0); PG8_BAR; PG8_MMA(0, 0, At, B0); PG8_MMA(0, 1, At, B1); PG8_BAR; PG8_SCHED;
	s_setprio 1
	s_waitcnt lgkmcnt(0)
	v_mfma_f32_16x16x32_bf16 v[60:63], v[152:155], v[196:199], v[60:63]
	v_mfma_f32_16x16x32_bf16 v[56:59], v[172:175], v[196:199], v[56:59]
	v_mfma_f32_16x16x32_bf16 v[40:43], v[152:155], v[204:207], v[40:43]
	v_mfma_f32_16x16x32_bf16 v[32:35], v[172:175], v[204:207], v[32:35]
	v_mfma_f32_16x16x32_bf16 v[24:27], v[152:155], v[212:215], v[24:27]
	v_mfma_f32_16x16x32_bf16 v[16:19], v[172:175], v[212:215], v[16:19]
	v_mfma_f32_16x16x32_bf16 v[4:7], v[152:155], v[220:223], v[4:7]
	v_mfma_f32_16x16x32_bf16 v[0:3], v[172:175], v[220:223], v[0:3]
	v_mfma_f32_16x16x32_bf16 v[60:63], v[168:171], v[200:203], v[60:63]
	v_mfma_f32_16x16x32_bf16 v[56:59], v[176:179], v[200:203], v[56:59]
	v_mfma_f32_16x16x32_bf16 v[40:43], v[168:171], v[208:211], v[40:43]
	v_mfma_f32_16x16x32_bf16 v[32:35], v[176:179], v[208:211], v[32:35]
	v_mfma_f32_16x16x32_bf16 v[24:27], v[168:171], v[216:219], v[24:27]
	v_mfma_f32_16x16x32_bf16 v[16:19], v[176:179], v[216:219], v[16:19]
	v_mfma_f32_16x16x32_bf16 v[4:7], v[168:171], v[226:229], v[4:7]
	v_mfma_f32_16x16x32_bf16 v[0:3], v[176:179], v[226:229], v[0:3]
	s_setprio 0
	s_setprio 1
	v_mfma_f32_16x16x32_bf16 v[52:55], v[180:183], v[196:199], v[52:55]
	v_mfma_f32_16x16x32_bf16 v[48:51], v[188:191], v[196:199], v[48:51]
	v_mfma_f32_16x16x32_bf16 v[44:47], v[180:183], v[204:207], v[44:47]
	v_mfma_f32_16x16x32_bf16 v[36:39], v[188:191], v[204:207], v[36:39]
	v_mfma_f32_16x16x32_bf16 v[28:31], v[180:183], v[212:215], v[28:31]
	v_mfma_f32_16x16x32_bf16 v[20:23], v[188:191], v[212:215], v[20:23]
	v_mfma_f32_16x16x32_bf16 v[12:15], v[180:183], v[220:223], v[12:15]
	v_mfma_f32_16x16x32_bf16 v[8:11], v[188:191], v[220:223], v[8:11]
	v_mfma_f32_16x16x32_bf16 v[52:55], v[184:187], v[200:203], v[52:55]
	v_mfma_f32_16x16x32_bf16 v[48:51], v[192:195], v[200:203], v[48:51]
	v_mfma_f32_16x16x32_bf16 v[44:47], v[184:187], v[208:211], v[44:47]
	v_mfma_f32_16x16x32_bf16 v[36:39], v[192:195], v[208:211], v[36:39]
	v_mfma_f32_16x16x32_bf16 v[28:31], v[184:187], v[216:219], v[28:31]
	v_mfma_f32_16x16x32_bf16 v[20:23], v[192:195], v[216:219], v[20:23]
	v_mfma_f32_16x16x32_bf16 v[12:15], v[184:187], v[226:229], v[12:15]
	v_mfma_f32_16x16x32_bf16 v[8:11], v[192:195], v[226:229], v[8:11]
	s_setprio 0
	s_barrier
	v_add_u32_e32 v64, s56, v161
	ds_read_b128 v[152:155], v64
	ds_read_b128 v[168:171], v64 offset:1024
	ds_read_b128 v[172:175], v64 offset:2048
	ds_read_b128 v[176:179], v64 offset:3072
	v_add_u32_e32 v64, s57, v161
	ds_read_b128 v[180:183], v64
	ds_read_b128 v[184:187], v64 offset:1024
	ds_read_b128 v[188:191], v64 offset:2048
	ds_read_b128 v[192:195], v64 offset:3072
	s_mov_b32 m0, s54
	v_cndmask_b32_e32 v64, v136, v165, vcc
	ds_read_b128 v[196:199], v162 offset:32768
	ds_read_b128 v[200:203], v162 offset:33792
	ds_read_b128 v[204:207], v162 offset:34816
	ds_read_b128 v[208:211], v162 offset:35840
	ds_read_b128 v[212:215], v162 offset:36864
	ds_read_b128 v[216:219], v162 offset:37888
	ds_read_b128 v[220:223], v162 offset:38912
	ds_read_b128 v[226:229], v162 offset:39936
	v_cndmask_b32_e32 v135, v134, v166, vcc
	global_load_lds_dwordx4 v64, s[34:35]
	s_mov_b32 m0, s55
	s_nop 0
	global_load_lds_dwordx4 v135, s[34:35]
	s_waitcnt vmcnt(8)
	s_waitcnt lgkmcnt(0)
	s_barrier
	s_setprio 1
	s_waitcnt lgkmcnt(0)
	v_mfma_f32_16x16x32_bf16 v[126:129], v[152:155], v[196:199], v[126:129]
	v_mfma_f32_16x16x32_bf16 v[122:125], v[172:175], v[196:199], v[122:125]
	v_mfma_f32_16x16x32_bf16 v[110:113], v[152:155], v[204:207], v[110:113]
	v_mfma_f32_16x16x32_bf16 v[106:109], v[172:175], v[204:207], v[106:109]
	v_mfma_f32_16x16x32_bf16 v[94:97], v[152:155], v[212:215], v[94:97]
	v_mfma_f32_16x16x32_bf16 v[90:93], v[172:175], v[212:215], v[90:93]
	v_mfma_f32_16x16x32_bf16 v[78:81], v[152:155], v[220:223], v[78:81]
	v_mfma_f32_16x16x32_bf16 v[74:77], v[172:175], v[220:223], v[74:77]
	v_mfma_f32_16x16x32_bf16 v[126:129], v[168:171], v[200:203], v[126:129]
	v_mfma_f32_16x16x32_bf16 v[122:125], v[176:179], v[200:203], v[122:125]
	v_mfma_f32_16x16x32_bf16 v[110:113], v[168:171], v[208:211], v[110:113]
	v_mfma_f32_16x16x32_bf16 v[106:109], v[176:179], v[208:211], v[106:109]
	v_mfma_f32_16x16x32_bf16 v[94:97], v[168:171], v[216:219], v[94:97]
	v_mfma_f32_16x16x32_bf16 v[90:93], v[176:179], v[216:219], v[90:93]
	v_mfma_f32_16x16x32_bf16 v[78:81], v[168:171], v[226:229], v[78:81]
	v_mfma_f32_16x16x32_bf16 v[74:77], v[176:179], v[226:229], v[74:77]
	s_setprio 0
	s_setprio 1
	v_mfma_f32_16x16x32_bf16 v[118:121], v[180:183], v[196:199], v[118:121]
	v_mfma_f32_16x16x32_bf16 v[114:117], v[188:191], v[196:199], v[114:117]
	v_mfma_f32_16x16x32_bf16 v[102:105], v[180:183], v[204:207], v[102:105]
	v_mfma_f32_16x16x32_bf16 v[98:101], v[188:191], v[204:207], v[98:101]
	v_mfma_f32_16x16x32_bf16 v[86:89], v[180:183], v[212:215], v[86:89]
	v_mfma_f32_16x16x32_bf16 v[82:85], v[188:191], v[212:215], v[82:85]
	v_mfma_f32_16x16x32_bf16 v[70:73], v[180:183], v[220:223], v[70:73]
	v_mfma_f32_16x16x32_bf16 v[66:69], v[188:191], v[220:223], v[66:69]
	v_mfma_f32_16x16x32_bf16 v[118:121], v[184:187], v[200:203], v[118:121]
	v_mfma_f32_16x16x32_bf16 v[114:117], v[192:195], v[200:203], v[114:117]
	v_mfma_f32_16x16x32_bf16 v[102:105], v[184:187], v[208:211], v[102:105]
	v_mfma_f32_16x16x32_bf16 v[98:101], v[192:195], v[208:211], v[98:101]
	v_mfma_f32_16x16x32_bf16 v[86:89], v[184:187], v[216:219], v[86:89]
	v_mfma_f32_16x16x32_bf16 v[82:85], v[192:195], v[216:219], v[82:85]
	v_mfma_f32_16x16x32_bf16 v[70:73], v[184:187], v[226:229], v[70:73]
	v_mfma_f32_16x16x32_bf16 v[66:69], v[192:195], v[226:229], v[66:69]
	s_setprio 0
	s_barrier
; #define PG8_STAGE_A(bufoff, kt, h, usenext) do { if constexpr (Sched::GATHER) { unsigned vo_[2] = { (usenext) ? goffN[h][0] : goff[h][0], (usenext) ? goffN[h][1] : goff[h][1] }; PG8_STAGE(bufoff, kt, vo_); } \
;         else { PG8_STAGE(bufoff, (kt) + ((h) ? hstep : 0), voffA); } } while (0)
; #define PG8_STAGE(bufoff, gbase, voff) do { _Pragma("unroll") for (int _i = 0; _i < 2; ++_i) \
;         __builtin_amdgcn_global_load_lds((const unsigned*)((const char*)(gbase) + (voff)[_i]), (LAS unsigned*)(lds + (bufoff) + ldsw + _i * 8192), 16, 0, 0); } while (0)
; template <class Epi, class Sched, bool ALIGN_EPI = true, bool SP2 = true>
; __device__ __forceinline__ void gemm_phase(LAS unsigned char* lds, const Gemm g, const Sched& S, const Epi& E, int tid_in) {
;     ...
;             PG8_LDA(At, 1, 1); PG8_STAGE(PG8_SB(1, 0), b3, voffB); PG8_STAGE(PG8_SB(1, 1), b3 + hstepB, voffB); PG8_STAGE_A(PG8_SA(1, 0), a3, 0, last);
;             PG8_WAIT_V(8); PG8_WAIT_L(0); PG8_BAR; PG8_MMA(1, 0, At, B0); PG8_MMA(1, 1, At, B1); PG8_BAR; PG8_SCHED;
;             } else {
;             PG8_LDB(B0, 0, 0); PG8_SCHED; PG8_LDA(At, 0, 0); PG8_STAGE_A(PG8_SA(1, 1), a1, 1, false);
;             PG8_WAIT_L(8); PG8_BAR; PG8_WAIT_L(0); PG8_MMA(0, 0, At, B0); PG8_BAR; PG8_SCHED;
;             PG8_LDB(B1, 0, 1); PG8_STAGE(PG8_SB(0, 0), b2, voffB);
;             PG8_BAR; PG8_WAIT_L(0); PG8_MMA(0, 1, At, B1); PG8_BAR;
;             PG8_LDA(At, 0, 1); PG8_STAGE_A(PG8_SA(0, 0), a2, 0, last);
;             PG8_BAR; PG8_WAIT_L(0); PG8_MMA(1, 0, At, B0); PG8_BAR; PG8_SCHED;
;             PG8_STAGE(PG8_SB(0, 1), b2 + hstepB, voffB);
;             PG8_WAIT_V(6); PG8_BAR; PG8_MMA(1, 1, At, B1); PG8_BAR;
;             PG8_LDB(B0, 1, 0); PG8_SCHED; PG8_LDA(At, 1, 0); PG8_STAGE_A(PG8_SA(0, 1), a2, 1, last);
;             PG8_WAIT_L(8); PG8_BAR; PG8_WAIT_L(0); PG8_MMA(0, 0, At, B0); PG8_BAR; PG8_SCHED;
;             PG8_LDB(B1, 1, 1); PG8_STAGE(PG8_SB(1, 0), b3, voffB);
;             PG8_BAR; PG8_WAIT_L(0); PG8_MMA(0, 1, At, B1); PG8_BAR;
;             PG8_LDA(At, 1, 1); PG8_STAGE_A(PG8_SA(1, 0), a3, 0, last);
;             PG8_BAR; PG8_WAIT_L(0); PG8_MMA(1, 0, At, B0); PG8_BAR; PG8_SCHED;
;             PG8_STAGE(PG8_SB(1, 1), b3 + hstepB, voffB);
;             PG8_WAIT_V(6); PG8_BAR; PG8_MMA(1, 1, At, B1); PG8_BAR;
;             }
;         }
;         if constexpr (ALIGN_EPI) { if (wr == 0) PG8_BAR; }
	s_mov_b32 m0, s58
	v_lshl_add_u64 v[148:149], v[148:149], 0, s[84:85]
	s_add_u32 s30, s30, 0x40080
	ds_read_b128 v[196:199], v162 offset:49152
	ds_read_b128 v[200:203], v162 offset:50176
	ds_read_b128 v[204:207], v162 offset:51200
	ds_read_b128 v[208:211], v162 offset:52224
	ds_read_b128 v[212:215], v162 offset:53248
	ds_read_b128 v[216:219], v162 offset:54272
	ds_read_b128 v[220:223], v162 offset:55296
	ds_read_b128 v[226:229], v162 offset:56320
	global_load_lds_dwordx4 v[148:149], off
	v_lshl_add_u64 v[148:149], v[234:235], 0, s[84:85]
	s_mov_b32 m0, s59
	s_addc_u32 s31, s31, 0
	global_load_lds_dwordx4 v[148:149], off
	v_lshl_add_u64 v[148:149], s[30:31], 0, v[130:131]
	s_mov_b32 m0, s62
	s_nop 0
	global_load_lds_dwordx4 v[148:149], off
	v_lshl_add_u64 v[148:149], s[30:31], 0, v[132:133]
	s_mov_b32 m0, s63
	s_nop 0
	global_load_lds_dwordx4 v[148:149], off
	v_lshl_add_u64 v[148:149], v[238:239], 0, s[84:85]
	s_mov_b32 m0, s60
	s_nop 0
	global_load_lds_dwordx4 v[148:149], off
	v_lshl_add_u64 v[148:149], v[236:237], 0, s[84:85]
	s_mov_b32 m0, s61
	s_nop 0
	global_load_lds_dwordx4 v[148:149], off
	s_waitcnt vmcnt(8)
	s_waitcnt lgkmcnt(0)
	s_barrier
	s_setprio 1
	s_waitcnt lgkmcnt(0)
	v_mfma_f32_16x16x32_bf16 v[60:63], v[152:155], v[196:199], v[60:63]
	v_mfma_f32_16x16x32_bf16 v[56:59], v[172:175], v[196:199], v[56:59]
	v_mfma_f32_16x16x32_bf16 v[40:43], v[152:155], v[204:207], v[40:43]
	v_mfma_f32_16x16x32_bf16 v[32:35], v[172:175], v[204:207], v[32:35]
	v_mfma_f32_16x16x32_bf16 v[24:27], v[152:155], v[212:215], v[24:27]
	v_mfma_f32_16x16x32_bf16 v[16:19], v[172:175], v[212:215], v[16:19]
	v_mfma_f32_16x16x32_bf16 v[4:7], v[152:155], v[220:223], v[4:7]
	v_mfma_f32_16x16x32_bf16 v[0:3], v[172:175], v[220:223], v[0:3]
	v_mfma_f32_16x16x32_bf16 v[60:63], v[168:171], v[200:203], v[60:63]
	v_mfma_f32_16x16x32_bf16 v[56:59], v[176:179], v[200:203], v[56:59]
	v_mfma_f32_16x16x32_bf16 v[40:43], v[168:171], v[208:211], v[40:43]
	v_mfma_f32_16x16x32_bf16 v[32:35], v[176:179], v[208:211], v[32:35]
	v_mfma_f32_16x16x32_bf16 v[24:27], v[168:171], v[216:219], v[24:27]
	v_mfma_f32_16x16x32_bf16 v[16:19], v[176:179], v[216:219], v[16:19]
	v_mfma_f32_16x16x32_bf16 v[4:7], v[168:171], v[226:229], v[4:7]
	v_mfma_f32_16x16x32_bf16 v[0:3], v[176:179], v[226:229], v[0:3]
	s_setprio 0
	s_setprio 1
	v_mfma_f32_16x16x32_bf16 v[52:55], v[180:183], v[196:199], v[52:55]
	v_mfma_f32_16x16x32_bf16 v[48:51], v[188:191], v[196:199], v[48:51]
	v_mfma_f32_16x16x32_bf16 v[44:47], v[180:183], v[204:207], v[44:47]
	v_mfma_f32_16x16x32_bf16 v[36:39], v[188:191], v[204:207], v[36:39]
	v_mfma_f32_16x16x32_bf16 v[28:31], v[180:183], v[212:215], v[28:31]
	v_mfma_f32_16x16x32_bf16 v[20:23], v[188:191], v[212:215], v[20:23]
	v_mfma_f32_16x16x32_bf16 v[12:15], v[180:183], v[220:223], v[12:15]
	v_mfma_f32_16x16x32_bf16 v[8:11], v[188:191], v[220:223], v[8:11]
	v_mfma_f32_16x16x32_bf16 v[52:55], v[184:187], v[200:203], v[52:55]
	v_mfma_f32_16x16x32_bf16 v[48:51], v[192:195], v[200:203], v[48:51]
	v_mfma_f32_16x16x32_bf16 v[44:47], v[184:187], v[208:211], v[44:47]
	v_mfma_f32_16x16x32_bf16 v[36:39], v[192:195], v[208:211], v[36:39]
	v_mfma_f32_16x16x32_bf16 v[28:31], v[184:187], v[216:219], v[28:31]
	v_mfma_f32_16x16x32_bf16 v[20:23], v[192:195], v[216:219], v[20:23]
	v_mfma_f32_16x16x32_bf16 v[12:15], v[184:187], v[226:229], v[12:15]
	v_mfma_f32_16x16x32_bf16 v[8:11], v[192:195], v[226:229], v[8:11]
	s_setprio 0
	s_add_i32 s69, s69, 2
	s_add_u32 s2, s2, 0x100
	s_addc_u32 s3, s3, 0
	s_cmp_gt_u32 s69, 13
	s_barrier
	s_cbranch_scc0 .LBB0_2933
	s_and_b64 vcc, exec, s[20:21]
	s_cbranch_vccz .LBB0_2936
	s_barrier

; #define PG8_STAGE_A(bufoff, kt, h, usenext) do { if constexpr (Sched::GATHER) { unsigned vo_[2] = { (usenext) ? goffN[h][0] : goff[h][0], (usenext) ? goffN[h][1] : goff[h][1] }; PG8_STAGE(bufoff, kt, vo_); } \
;         else { PG8_STAGE(bufoff, (kt) + ((h) ? hstep : 0), voffA); } } while (0)
; #define PG8_STAGE(bufoff, gbase, voff) do { _Pragma("unroll") for (int _i = 0; _i < 2; ++_i) \
;         __builtin_amdgcn_global_load_lds((const unsigned*)((const char*)(gbase) + (voff)[_i]), (LAS unsigned*)(lds + (bufoff) + ldsw + _i * 8192), 16, 0, 0); } while (0)
; #define PG8_LDA(dst, b, h) do { _Pragma("unroll") for (int m = 0; m < 4; ++m) _Pragma("unroll") for (int k = 0; k < 2; ++k) dst[m][k] = *(const LAS bf16x8*)(lds + PG8_SA(b, h) + aoff + m * 2048 + k * 1024); } while (0)
; #define PG8_LDB(dst, b, h) do { _Pragma("unroll") for (int n = 0; n < 2; ++n) _Pragma("unroll") for (int k = 0; k < 2; ++k) dst[n][k] = *(const LAS bf16x8*)(lds + PG8_SB(b, h) + boff + n * 2048 + k * 1024); } while (0)
; #define PG8_MMA(ai, bj, At, Bt) do { __builtin_amdgcn_s_setprio(1); _Pragma("unroll") for (int m = 0; m < 4; ++m) _Pragma("unroll") for (int n = 0; n < 2; ++n) _Pragma("unroll") for (int k = 0; k < 2; ++k) \
;         acc[ai][bj][m][n] = __builtin_amdgcn_mfma_f32_16x16x32_bf16(Bt[n][k], At[m][k], acc[ai][bj][m][n], 0, 0, 0); __builtin_amdgcn_s_setprio(0); } while (0)
; #define PG8_WAIT_V(n) asm volatile("s_waitcnt vmcnt(" #n ")" ::: "memory")
; template <class Epi, class Sched, bool ALIGN_EPI = true, bool SP2 = true>
; __device__ __forceinline__ void gemm_phase(LAS unsigned char* lds, const Gemm g, const Sched& S, const Epi& E, int tid_in) {
;     ...
;             const char* a1 = cA + (size_t)(t + 1) * kstep;
;             const char* a2 = last ? nA : cA + (size_t)(t + 2) * kstep; const char* b2 = last ? nB : cB + (size_t)(t + 2) * kstep;
;             const char* a3 = a2 + kstep; const char* b3 = b2 + kstep;
;             if constexpr (SP2) {
;             PG8_LDB(B0, 0, 0); PG8_LDB(B1, 0, 1); PG8_SCHED; PG8_LDA(At, 0, 0); PG8_STAGE_A(PG8_SA(1, 1), a1, 1, false);
;             PG8_WAIT_V(8); PG8_WAIT_L(0); PG8_BAR; PG8_MMA(0, 0, At, B0); PG8_MMA(0, 1, At, B1); PG8_BAR; PG8_SCHED;
;             PG8_LDA(At, 0, 1); PG8_STAGE(PG8_SB(0, 0), b2, voffB); PG8_STAGE(PG8_SB(0, 1), b2 + hstepB, voffB); PG8_STAGE_A(PG8_SA(0, 0), a2, 0, last);
.LBB0_3014:
	v_add_u32_e32 v156, s41, v141
	v_add_u32_e32 v172, s42, v141
	ds_read_b128 v[144:147], v156
	ds_read_b128 v[148:151], v156 offset:1024
	ds_read_b128 v[152:155], v156 offset:2048
	ds_read_b128 v[156:159], v156 offset:3072
	ds_read_b128 v[160:163], v172
	ds_read_b128 v[164:167], v172 offset:1024
	ds_read_b128 v[168:171], v172 offset:2048
	ds_read_b128 v[172:175], v172 offset:3072
	s_add_u32 s24, s22, 0xfffe0080
	s_addc_u32 s25, s23, -1
	s_cmp_eq_u32 s67, 4
	s_cselect_b32 s27, s15, s25
	s_cselect_b32 s26, s63, s24
	s_cselect_b32 s25, s17, s66
	s_cselect_b32 s24, s64, s65
	v_lshl_add_u64 v[208:209], s[22:23], 0, v[136:137]
	s_add_i32 m0, s47, 0xc000
	ds_read_b128 v[176:179], v143
	ds_read_b128 v[180:183], v143 offset:1024
	ds_read_b128 v[184:187], v143 offset:2048
	ds_read_b128 v[188:191], v143 offset:3072
	ds_read_b128 v[192:195], v143 offset:4096
	ds_read_b128 v[196:199], v143 offset:5120
	ds_read_b128 v[200:203], v143 offset:6144
	ds_read_b128 v[204:207], v143 offset:7168
	global_load_lds_dwordx4 v[208:209], off
	v_lshl_add_u64 v[208:209], s[22:23], 0, v[138:139]
	s_add_i32 m0, s47, 0xe000
	s_nop 0
	global_load_lds_dwordx4 v[208:209], off
	s_waitcnt vmcnt(8)
	s_waitcnt lgkmcnt(0)
	s_barrier
	s_setprio 1
	s_waitcnt lgkmcnt(0)
	v_mfma_f32_16x16x32_bf16 v[126:129], v[144:147], v[176:179], v[126:129]
	v_mfma_f32_16x16x32_bf16 v[122:125], v[152:155], v[176:179], v[122:125]
	v_mfma_f32_16x16x32_bf16 v[118:121], v[144:147], v[184:187], v[118:121]
	v_mfma_f32_16x16x32_bf16 v[114:117], v[152:155], v[184:187], v[114:117]
	v_mfma_f32_16x16x32_bf16 v[102:105], v[144:147], v[192:195], v[102:105]
	v_mfma_f32_16x16x32_bf16 v[98:101], v[152:155], v[192:195], v[98:101]
	v_mfma_f32_16x16x32_bf16 v[86:89], v[144:147], v[200:203], v[86:89]
	v_mfma_f32_16x16x32_bf16 v[82:85], v[152:155], v[200:203], v[82:85]
	v_mfma_f32_16x16x32_bf16 v[126:129], v[148:151], v[180:183], v[126:129]
	v_mfma_f32_16x16x32_bf16 v[122:125], v[156:159], v[180:183], v[122:125]
	v_mfma_f32_16x16x32_bf16 v[118:121], v[148:151], v[188:191], v[118:121]
	v_mfma_f32_16x16x32_bf16 v[114:117], v[156:159], v[188:191], v[114:117]
	v_mfma_f32_16x16x32_bf16 v[102:105], v[148:151], v[196:199], v[102:105]
	v_mfma_f32_16x16x32_bf16 v[98:101], v[156:159], v[196:199], v[98:101]
	v_mfma_f32_16x16x32_bf16 v[86:89], v[148:151], v[204:207], v[86:89]
	v_mfma_f32_16x16x32_bf16 v[82:85], v[156:159], v[204:207], v[82:85]
	s_setprio 0
	s_setprio 1
	v_mfma_f32_16x16x32_bf16 v[110:113], v[160:163], v[176:179], v[110:113]
	v_mfma_f32_16x16x32_bf16 v[106:109], v[168:171], v[176:179], v[106:109]
	v_mfma_f32_16x16x32_bf16 v[94:97], v[160:163], v[184:187], v[94:97]
	v_mfma_f32_16x16x32_bf16 v[90:93], v[168:171], v[184:187], v[90:93]
	v_mfma_f32_16x16x32_bf16 v[78:81], v[160:163], v[192:195], v[78:81]
	v_mfma_f32_16x16x32_bf16 v[74:77], v[168:171], v[192:195], v[74:77]
	v_mfma_f32_16x16x32_bf16 v[70:73], v[160:163], v[200:203], v[70:73]
	v_mfma_f32_16x16x32_bf16 v[66:69], v[168:171], v[200:203], v[66:69]
	v_mfma_f32_16x16x32_bf16 v[110:113], v[164:167], v[180:183], v[110:113]
	v_mfma_f32_16x16x32_bf16 v[106:109], v[172:175], v[180:183], v[106:109]
	v_mfma_f32_16x16x32_bf16 v[94:97], v[164:167], v[188:191], v[94:97]
	v_mfma_f32_16x16x32_bf16 v[90:93], v[172:175], v[188:191], v[90:93]
	v_mfma_f32_16x16x32_bf16 v[78:81], v[164:167], v[196:199], v[78:81]
	v_mfma_f32_16x16x32_bf16 v[74:77], v[172:175], v[196:199], v[74:77]
	v_mfma_f32_16x16x32_bf16 v[70:73], v[164:167], v[204:207], v[70:73]
	v_mfma_f32_16x16x32_bf16 v[66:69], v[172:175], v[204:207], v[66:69]
	s_setprio 0
	s_barrier
	s_mov_b32 m0, s11
	v_lshl_add_u64 v[208:209], s[24:25], 0, v[64:65]
	s_add_u32 s68, s24, 0x20000
	ds_read_b128 v[176:179], v143 offset:16384
	ds_read_b128 v[180:183], v143 offset:17408
	ds_read_b128 v[184:187], v143 offset:18432
	ds_read_b128 v[188:191], v143 offset:19456
	ds_read_b128 v[192:195], v143 offset:20480
	ds_read_b128 v[196:199], v143 offset:21504
	ds_read_b128 v[200:203], v143 offset:22528
	ds_read_b128 v[204:207], v143 offset:23552
	global_load_lds_dwordx4 v[208:209], off
	v_lshl_add_u64 v[210:211], s[24:25], 0, v[134:135]
	s_mov_b32 m0, s43
	s_addc_u32 s69, s25, 0
	global_load_lds_dwordx4 v[210:211], off
	v_lshl_add_u64 v[212:213], s[68:69], 0, v[64:65]
	s_mov_b32 m0, s44
	v_lshl_add_u64 v[214:215], s[26:27], 0, v[132:133]
	global_load_lds_dwordx4 v[212:213], off
	v_lshl_add_u64 v[212:213], s[68:69], 0, v[134:135]
	s_mov_b32 m0, s46
	s_nop 0
	global_load_lds_dwordx4 v[212:213], off
	v_lshl_add_u64 v[212:213], s[26:27], 0, v[130:131]
	s_mov_b32 m0, s47
	s_nop 0
	global_load_lds_dwordx4 v[212:213], off
	s_mov_b32 m0, s48
	s_nop 0
	global_load_lds_dwordx4 v[214:215], off
	s_waitcnt vmcnt(8)
	s_waitcnt lgkmcnt(0)
	s_barrier
; #define PG8_STAGE_A(bufoff, kt, h, usenext) do { if constexpr (Sched::GATHER) { unsigned vo_[2] = { (usenext) ? goffN[h][0] : goff[h][0], (usenext) ? goffN[h][1] : goff[h][1] }; PG8_STAGE(bufoff, kt, vo_); } \
;         else { PG8_STAGE(bufoff, (kt) + ((h) ? hstep : 0), voffA); } } while (0)
; #define PG8_LDA(dst, b, h) do { _Pragma("unroll") for (int m = 0; m < 4; ++m) _Pragma("unroll") for (int k = 0; k < 2; ++k) dst[m][k] = *(const LAS bf16x8*)(lds + PG8_SA(b, h) + aoff + m * 2048 + k * 1024); } while (0)
; #define PG8_LDB(dst, b, h) do { _Pragma("unroll") for (int n = 0; n < 2; ++n) _Pragma("unroll") for (int k = 0; k < 2; ++k) dst[n][k] = *(const LAS bf16x8*)(lds + PG8_SB(b, h) + boff + n * 2048 + k * 1024); } while (0)
; #define PG8_MMA(ai, bj, At, Bt) do { __builtin_amdgcn_s_setprio(1); _Pragma("unroll") for (int m = 0; m < 4; ++m) _Pragma("unroll") for (int n = 0; n < 2; ++n) _Pragma("unroll") for (int k = 0; k < 2; ++k) \
;         acc[ai][bj][m][n] = __builtin_amdgcn_mfma_f32_16x16x32_bf16(Bt[n][k], At[m][k], acc[ai][bj][m][n], 0, 0, 0); __builtin_amdgcn_s_setprio(0); } while (0)
; #define PG8_WAIT_V(n) asm volatile("s_waitcnt vmcnt(" #n ")" ::: "memory")
; #define PG8_WAIT_L(n) asm volatile("s_waitcnt lgkmcnt(" #n ")" ::: "memory")
; #define PG8_BAR __builtin_amdgcn_s_barrier()
; #define PG8_SCHED __builtin_amdgcn_sched_barrier(0)
; template <class Epi, class Sched, bool ALIGN_EPI = true, bool SP2 = true>
; __device__ __forceinline__ void gemm_phase(LAS unsigned char* lds, const Gemm g, const Sched& S, const Epi& E, int tid_in) {
;     ...
;             PG8_WAIT_V(8); PG8_WAIT_L(0); PG8_BAR; PG8_MMA(1, 0, At, B0); PG8_MMA(1, 1, At, B1); PG8_BAR; PG8_SCHED;
;             PG8_LDB(B0, 1, 0); PG8_LDB(B1, 1, 1); PG8_SCHED; PG8_LDA(At, 1, 0); PG8_STAGE_A(PG8_SA(0, 1), a2, 1, last);
;             PG8_WAIT_V(8); PG8_WAIT_L(0); PG8_BAR; PG8_MMA(0, 0, At, B0); PG8_MMA(0, 1, At, B1); PG8_BAR; PG8_SCHED;
	s_setprio 1
	s_waitcnt lgkmcnt(0)
	v_mfma_f32_16x16x32_bf16 v[60:63], v[144:147], v[176:179], v[60:63]
	v_mfma_f32_16x16x32_bf16 v[56:59], v[152:155], v[176:179], v[56:59]
	v_mfma_f32_16x16x32_bf16 v[52:55], v[144:147], v[184:187], v[52:55]
	v_mfma_f32_16x16x32_bf16 v[48:51], v[152:155], v[184:187], v[48:51]
	v_mfma_f32_16x16x32_bf16 v[36:39], v[144:147], v[192:195], v[36:39]
	v_mfma_f32_16x16x32_bf16 v[32:35], v[152:155], v[192:195], v[32:35]
	v_mfma_f32_16x16x32_bf16 v[20:23], v[144:147], v[200:203], v[20:23]
	v_mfma_f32_16x16x32_bf16 v[16:19], v[152:155], v[200:203], v[16:19]
	v_mfma_f32_16x16x32_bf16 v[60:63], v[148:151], v[180:183], v[60:63]
	v_mfma_f32_16x16x32_bf16 v[56:59], v[156:159], v[180:183], v[56:59]
	v_mfma_f32_16x16x32_bf16 v[52:55], v[148:151], v[188:191], v[52:55]
	v_mfma_f32_16x16x32_bf16 v[48:51], v[156:159], v[188:191], v[48:51]
	v_mfma_f32_16x16x32_bf16 v[36:39], v[148:151], v[196:199], v[36:39]
	v_mfma_f32_16x16x32_bf16 v[32:35], v[156:159], v[196:199], v[32:35]
	v_mfma_f32_16x16x32_bf16 v[20:23], v[148:151], v[204:207], v[20:23]
	v_mfma_f32_16x16x32_bf16 v[16:19], v[156:159], v[204:207], v[16:19]
	s_setprio 0
	s_setprio 1
	v_mfma_f32_16x16x32_bf16 v[44:47], v[160:163], v[176:179], v[44:47]
	v_mfma_f32_16x16x32_bf16 v[40:43], v[168:171], v[176:179], v[40:43]
	v_mfma_f32_16x16x32_bf16 v[28:31], v[160:163], v[184:187], v[28:31]
	v_mfma_f32_16x16x32_bf16 v[24:27], v[168:171], v[184:187], v[24:27]
	v_mfma_f32_16x16x32_bf16 v[12:15], v[160:163], v[192:195], v[12:15]
	v_mfma_f32_16x16x32_bf16 v[8:11], v[168:171], v[192:195], v[8:11]
	v_mfma_f32_16x16x32_bf16 v[4:7], v[160:163], v[200:203], v[4:7]
	v_mfma_f32_16x16x32_bf16 v[0:3], v[168:171], v[200:203], v[0:3]
	v_mfma_f32_16x16x32_bf16 v[44:47], v[164:167], v[180:183], v[44:47]
	v_mfma_f32_16x16x32_bf16 v[40:43], v[172:175], v[180:183], v[40:43]
	v_mfma_f32_16x16x32_bf16 v[28:31], v[164:167], v[188:191], v[28:31]
	v_mfma_f32_16x16x32_bf16 v[24:27], v[172:175], v[188:191], v[24:27]
	v_mfma_f32_16x16x32_bf16 v[12:15], v[164:167], v[196:199], v[12:15]
	v_mfma_f32_16x16x32_bf16 v[8:11], v[172:175], v[196:199], v[8:11]
	v_mfma_f32_16x16x32_bf16 v[4:7], v[164:167], v[204:207], v[4:7]
	v_mfma_f32_16x16x32_bf16 v[0:3], v[172:175], v[204:207], v[0:3]
	s_setprio 0
	s_barrier
	v_add_u32_e32 v156, s51, v141
	v_add_u32_e32 v172, s52, v141
	ds_read_b128 v[144:147], v156
	ds_read_b128 v[148:151], v156 offset:1024
	ds_read_b128 v[152:155], v156 offset:2048
	ds_read_b128 v[156:159], v156 offset:3072
	ds_read_b128 v[160:163], v172
	ds_read_b128 v[164:167], v172 offset:1024
	ds_read_b128 v[168:171], v172 offset:2048
	ds_read_b128 v[172:175], v172 offset:3072
	s_add_u32 s26, s26, 0x20000
	s_addc_u32 s27, s27, 0
	s_mov_b32 m0, s49
	v_lshl_add_u64 v[216:217], s[26:27], 0, v[130:131]
	ds_read_b128 v[176:179], v143 offset:32768
	ds_read_b128 v[180:183], v143 offset:33792
	ds_read_b128 v[184:187], v143 offset:34816
	ds_read_b128 v[188:191], v143 offset:35840
	ds_read_b128 v[192:195], v143 offset:36864
	ds_read_b128 v[196:199], v143 offset:37888
	ds_read_b128 v[200:203], v143 offset:38912
	ds_read_b128 v[204:207], v143 offset:39936
	global_load_lds_dwordx4 v[216:217], off
	v_lshl_add_u64 v[216:217], s[26:27], 0, v[132:133]
	s_mov_b32 m0, s50
	s_nop 0
	global_load_lds_dwordx4 v[216:217], off
	s_waitcnt vmcnt(8)
	s_waitcnt lgkmcnt(0)
	s_barrier
	s_setprio 1
	s_waitcnt lgkmcnt(0)
	v_mfma_f32_16x16x32_bf16 v[126:129], v[144:147], v[176:179], v[126:129]
	v_mfma_f32_16x16x32_bf16 v[122:125], v[152:155], v[176:179], v[122:125]
	v_mfma_f32_16x16x32_bf16 v[118:121], v[144:147], v[184:187], v[118:121]
	v_mfma_f32_16x16x32_bf16 v[114:117], v[152:155], v[184:187], v[114:117]
	v_mfma_f32_16x16x32_bf16 v[102:105], v[144:147], v[192:195], v[102:105]
	v_mfma_f32_16x16x32_bf16 v[98:101], v[152:155], v[192:195], v[98:101]
	v_mfma_f32_16x16x32_bf16 v[86:89], v[144:147], v[200:203], v[86:89]
	v_mfma_f32_16x16x32_bf16 v[82:85], v[152:155], v[200:203], v[82:85]
	v_mfma_f32_16x16x32_bf16 v[126:129], v[148:151], v[180:183], v[126:129]
	v_mfma_f32_16x16x32_bf16 v[122:125], v[156:159], v[180:183], v[122:125]
	v_mfma_f32_16x16x32_bf16 v[118:121], v[148:151], v[188:191], v[118:121]
	v_mfma_f32_16x16x32_bf16 v[114:117], v[156:159], v[188:191], v[114:117]
	v_mfma_f32_16x16x32_bf16 v[102:105], v[148:151], v[196:199], v[102:105]
	v_mfma_f32_16x16x32_bf16 v[98:101], v[156:159], v[196:199], v[98:101]
	v_mfma_f32_16x16x32_bf16 v[86:89], v[148:151], v[204:207], v[86:89]
	v_mfma_f32_16x16x32_bf16 v[82:85], v[156:159], v[204:207], v[82:85]
	s_setprio 0
	s_setprio 1
	v_mfma_f32_16x16x32_bf16 v[110:113], v[160:163], v[176:179], v[110:113]
	v_mfma_f32_16x16x32_bf16 v[106:109], v[168:171], v[176:179], v[106:109]
	v_mfma_f32_16x16x32_bf16 v[94:97], v[160:163], v[184:187], v[94:97]
	v_mfma_f32_16x16x32_bf16 v[90:93], v[168:171], v[184:187], v[90:93]
	v_mfma_f32_16x16x32_bf16 v[78:81], v[160:163], v[192:195], v[78:81]
	v_mfma_f32_16x16x32_bf16 v[74:77], v[168:171], v[192:195], v[74:77]
	v_mfma_f32_16x16x32_bf16 v[70:73], v[160:163], v[200:203], v[70:73]
	v_mfma_f32_16x16x32_bf16 v[66:69], v[168:171], v[200:203], v[66:69]
	v_mfma_f32_16x16x32_bf16 v[110:113], v[164:167], v[180:183], v[110:113]
	v_mfma_f32_16x16x32_bf16 v[106:109], v[172:175], v[180:183], v[106:109]
	v_mfma_f32_16x16x32_bf16 v[94:97], v[164:167], v[188:191], v[94:97]
	v_mfma_f32_16x16x32_bf16 v[90:93], v[172:175], v[188:191], v[90:93]
	v_mfma_f32_16x16x32_bf16 v[78:81], v[164:167], v[196:199], v[78:81]
	v_mfma_f32_16x16x32_bf16 v[74:77], v[172:175], v[196:199], v[74:77]
	v_mfma_f32_16x16x32_bf16 v[70:73], v[164:167], v[204:207], v[70:73]
	v_mfma_f32_16x16x32_bf16 v[66:69], v[172:175], v[204:207], v[66:69]
	s_setprio 0
	s_barrier
; #define PG8_STAGE_A(bufoff, kt, h, usenext) do { if constexpr (Sched::GATHER) { unsigned vo_[2] = { (usenext) ? goffN[h][0] : goff[h][0], (usenext) ? goffN[h][1] : goff[h][1] }; PG8_STAGE(bufoff, kt, vo_); } \
;         else { PG8_STAGE(bufoff, (kt) + ((h) ? hstep : 0), voffA); } } while (0)
; #define PG8_STAGE(bufoff, gbase, voff) do { _Pragma("unroll") for (int _i = 0; _i < 2; ++_i) \
;         __builtin_amdgcn_global_load_lds((const unsigned*)((const char*)(gbase) + (voff)[_i]), (LAS unsigned*)(lds + (bufoff) + ldsw + _i * 8192), 16, 0, 0); } while (0)
; #define PG8_LDA(dst, b, h) do { _Pragma("unroll") for (int m = 0; m < 4; ++m) _Pragma("unroll") for (int k = 0; k < 2; ++k) dst[m][k] = *(const LAS bf16x8*)(lds + PG8_SA(b, h) + aoff + m * 2048 + k * 1024); } while (0)
; #define PG8_MMA(ai, bj, At, Bt) do { __builtin_amdgcn_s_setprio(1); _Pragma("unroll") for (int m = 0; m < 4; ++m) _Pragma("unroll") for (int n = 0; n < 2; ++n) _Pragma("unroll") for (int k = 0; k < 2; ++k) \
;         acc[ai][bj][m][n] = __builtin_amdgcn_mfma_f32_16x16x32_bf16(Bt[n][k], At[m][k], acc[ai][bj][m][n], 0, 0, 0); __builtin_amdgcn_s_setprio(0); } while (0)
; #define PG8_WAIT_V(n) asm volatile("s_waitcnt vmcnt(" #n ")" ::: "memory")
; #define PG8_WAIT_L(n) asm volatile("s_waitcnt lgkmcnt(" #n ")" ::: "memory")
; #define PG8_BAR __builtin_amdgcn_s_barrier()
; #define PG8_SCHED __builtin_amdgcn_sched_barrier(0)
; template <class Epi, class Sched, bool ALIGN_EPI = true, bool SP2 = true>
; __device__ __forceinline__ void gemm_phase(LAS unsigned char* lds, const Gemm g, const Sched& S, const Epi& E, int tid_in) {
;     ...
;         for (int t = 0; t < nt; t += 2) {
;             if constexpr (Epi::HAS_MID) { if (t == nt / 2) E.mid(acc, cur, wr, wc, fr, fq); }
;             const bool last = (t == nt - 2);
;             const char* a1 = cA + (size_t)(t + 1) * kstep;
;             const char* a2 = last ? nA : cA + (size_t)(t + 2) * kstep; const char* b2 = last ? nB : cB + (size_t)(t + 2) * kstep;
;             const char* a3 = a2 + kstep; const char* b3 = b2 + kstep;
;     ...
;             PG8_LDA(At, 1, 1); PG8_STAGE(PG8_SB(1, 0), b3, voffB); PG8_STAGE(PG8_SB(1, 1), b3 + hstepB, voffB); PG8_STAGE_A(PG8_SA(1, 0), a3, 0, last);
;             PG8_WAIT_V(8); PG8_WAIT_L(0); PG8_BAR; PG8_MMA(1, 0, At, B0); PG8_MMA(1, 1, At, B1); PG8_BAR; PG8_SCHED;
	s_mov_b32 m0, s55
	v_lshl_add_u64 v[208:209], v[208:209], 0, s[84:85]
	s_add_u32 s24, s24, 0x20080
	ds_read_b128 v[176:179], v143 offset:49152
	ds_read_b128 v[180:183], v143 offset:50176
	ds_read_b128 v[184:187], v143 offset:51200
	ds_read_b128 v[188:191], v143 offset:52224
	ds_read_b128 v[192:195], v143 offset:53248
	ds_read_b128 v[196:199], v143 offset:54272
	ds_read_b128 v[200:203], v143 offset:55296
	ds_read_b128 v[204:207], v143 offset:56320
	global_load_lds_dwordx4 v[208:209], off
	v_lshl_add_u64 v[208:209], v[210:211], 0, s[84:85]
	s_mov_b32 m0, s56
	s_addc_u32 s25, s25, 0
	global_load_lds_dwordx4 v[208:209], off
	v_lshl_add_u64 v[208:209], s[24:25], 0, v[64:65]
	s_mov_b32 m0, s59
	s_nop 0
	global_load_lds_dwordx4 v[208:209], off
	v_lshl_add_u64 v[208:209], s[24:25], 0, v[134:135]
	s_mov_b32 m0, s60
	s_nop 0
	global_load_lds_dwordx4 v[208:209], off
	v_lshl_add_u64 v[208:209], v[212:213], 0, s[84:85]
	s_mov_b32 m0, s57
	s_nop 0
	global_load_lds_dwordx4 v[208:209], off
	v_lshl_add_u64 v[208:209], v[214:215], 0, s[84:85]
	s_mov_b32 m0, s58
	s_nop 0
	global_load_lds_dwordx4 v[208:209], off
	s_waitcnt vmcnt(8)
	s_waitcnt lgkmcnt(0)
	s_barrier
	s_setprio 1
	s_waitcnt lgkmcnt(0)
	v_mfma_f32_16x16x32_bf16 v[60:63], v[144:147], v[176:179], v[60:63]
	v_mfma_f32_16x16x32_bf16 v[56:59], v[152:155], v[176:179], v[56:59]
	v_mfma_f32_16x16x32_bf16 v[52:55], v[144:147], v[184:187], v[52:55]
	v_mfma_f32_16x16x32_bf16 v[48:51], v[152:155], v[184:187], v[48:51]
	v_mfma_f32_16x16x32_bf16 v[36:39], v[144:147], v[192:195], v[36:39]
	v_mfma_f32_16x16x32_bf16 v[32:35], v[152:155], v[192:195], v[32:35]
	v_mfma_f32_16x16x32_bf16 v[20:23], v[144:147], v[200:203], v[20:23]
	v_mfma_f32_16x16x32_bf16 v[16:19], v[152:155], v[200:203], v[16:19]
	v_mfma_f32_16x16x32_bf16 v[60:63], v[148:151], v[180:183], v[60:63]
	v_mfma_f32_16x16x32_bf16 v[56:59], v[156:159], v[180:183], v[56:59]
	v_mfma_f32_16x16x32_bf16 v[52:55], v[148:151], v[188:191], v[52:55]
	v_mfma_f32_16x16x32_bf16 v[48:51], v[156:159], v[188:191], v[48:51]
	v_mfma_f32_16x16x32_bf16 v[36:39], v[148:151], v[196:199], v[36:39]
	v_mfma_f32_16x16x32_bf16 v[32:35], v[156:159], v[196:199], v[32:35]
	v_mfma_f32_16x16x32_bf16 v[20:23], v[148:151], v[204:207], v[20:23]
	v_mfma_f32_16x16x32_bf16 v[16:19], v[156:159], v[204:207], v[16:19]
	s_setprio 0
	s_setprio 1
	v_mfma_f32_16x16x32_bf16 v[44:47], v[160:163], v[176:179], v[44:47]
	v_mfma_f32_16x16x32_bf16 v[40:43], v[168:171], v[176:179], v[40:43]
	v_mfma_f32_16x16x32_bf16 v[28:31], v[160:163], v[184:187], v[28:31]
	v_mfma_f32_16x16x32_bf16 v[24:27], v[168:171], v[184:187], v[24:27]
	v_mfma_f32_16x16x32_bf16 v[12:15], v[160:163], v[192:195], v[12:15]
	v_mfma_f32_16x16x32_bf16 v[8:11], v[168:171], v[192:195], v[8:11]
	v_mfma_f32_16x16x32_bf16 v[4:7], v[160:163], v[200:203], v[4:7]
	v_mfma_f32_16x16x32_bf16 v[0:3], v[168:171], v[200:203], v[0:3]
	v_mfma_f32_16x16x32_bf16 v[44:47], v[164:167], v[180:183], v[44:47]
	v_mfma_f32_16x16x32_bf16 v[40:43], v[172:175], v[180:183], v[40:43]
	v_mfma_f32_16x16x32_bf16 v[28:31], v[164:167], v[188:191], v[28:31]
	v_mfma_f32_16x16x32_bf16 v[24:27], v[172:175], v[188:191], v[24:27]
	v_mfma_f32_16x16x32_bf16 v[12:15], v[164:167], v[196:199], v[12:15]
	v_mfma_f32_16x16x32_bf16 v[8:11], v[172:175], v[196:199], v[8:11]
	v_mfma_f32_16x16x32_bf16 v[4:7], v[164:167], v[204:207], v[4:7]
	v_mfma_f32_16x16x32_bf16 v[0:3], v[172:175], v[204:207], v[0:3]
	s_setprio 0
	s_add_i32 s67, s67, 2
	s_add_u32 s22, s22, 0x100
	s_addc_u32 s23, s23, 0
	s_add_u32 s65, s65, 0x100
	s_addc_u32 s66, s66, 0
	s_cmp_gt_u32 s67, 5
	s_barrier
	s_cbranch_scc0 .LBB0_3014
	s_and_b64 vcc, exec, s[12:13]
	s_cbranch_vccz .LBB0_3017
	s_barrier
